# conversion plan re-partitioned: no conversion WGs in MoE-down-0 (256 GEMM WGs), L1-down converted in MoE-up-0, gate/up ranges shifted to in-proj-0/out-proj-0
# speedup vs baseline: 1.0046x; 1.0046x over previous
.LBB0_254:
	s_load_dwordx4 s[0:3], s[8:9], 0x138
	s_waitcnt lgkmcnt(0)
	s_mov_b64 s[4:5], s[0:1]
	s_cmp_lt_i32 s4, 3
	s_cselect_b64 s[0:1], -1, 0
	s_cmp_gt_i32 s5, 2
	s_cselect_b64 s[2:3], -1, 0
	s_and_b64 s[0:1], s[0:1], s[2:3]
	s_andn2_b64 vcc, exec, s[0:1]
	s_cbranch_vccnz .LBB0_356
	s_mov_b64 s[0:1], s[8:9]
	v_mbcnt_lo_u32_b32 v152, -1, 0
	v_mbcnt_hi_u32_b32 v152, -1, v152
	s_load_dword s38, s[8:9], 0x148
	s_add_u32 s2, s8, 0x148
	v_readlane_b32 s4, v243, 0
	s_addc_u32 s3, s9, 0
	v_readlane_b32 s5, v243, 1
	s_waitcnt lgkmcnt(0)
	s_sub_i32 s39, s38, 40
	s_cmp_lt_i32 s4, s39
	s_mov_b64 s[4:5], -1
	s_cbranch_scc1 .LBB0_276
	v_readlane_b32 s4, v243, 0
	s_sub_i32 s4, s4, s39
	s_lshl_b32 s6, s4, 3
	s_add_i32 s6, s6, s94
	s_cmpk_gt_u32 s6, 0x35ff
	v_readlane_b32 s5, v243, 1
	s_cbranch_scc1 .LBB0_275
	s_bitcmp0_b32 s6, 8
	s_movk_i32 s12, 0xf8
	s_cselect_b32 s4, s12, 0x108
	s_add_u32 s4, s0, s4
	s_addc_u32 s5, s1, 0
	s_load_dwordx2 s[8:9], s[4:5], 0x0
	s_load_dwordx2 s[10:11], s[0:1], 0x130
	s_lshl_b32 s4, s6, 13
	s_and_b32 s4, s4, 0x7c00000
	v_lshlrev_b32_e32 v0, 1, v152
	s_waitcnt lgkmcnt(0)
	s_add_u32 s8, s8, s4
	s_addc_u32 s9, s9, 0
	s_lshl_b32 s4, s6, 2
	s_and_b32 s4, s4, 0x380
	v_and_b32_e32 v132, -16, v0
	v_add_u32_e32 v0, s4, v132
	v_ashrrev_i32_e32 v1, 31, v0
	v_lshlrev_b64 v[0:1], 12, v[0:1]
	s_lshl_b32 s4, s6, 7
	v_lshlrev_b32_e32 v2, 2, v152
	s_mov_b32 s5, 0
	v_lshl_add_u64 v[0:1], s[8:9], 0, v[0:1]
	s_and_b32 s4, s4, 0xf80
	v_and_b32_e32 v134, 28, v2
	v_lshl_add_u64 v[0:1], v[0:1], 0, s[4:5]
	v_mov_b32_e32 v137, 0
	v_lshlrev_b32_e32 v136, 2, v134
	v_lshl_add_u64 v[56:57], v[0:1], 0, v[136:137]
	s_mov_b32 s4, 0x5001000
	v_add_co_u32_e32 v4, vcc, s4, v56
	s_mov_b32 s4, 0x5003000
	s_nop 0
	v_addc_co_u32_e32 v5, vcc, 0, v57, vcc
	v_add_co_u32_e32 v12, vcc, s4, v56
	s_mov_b32 s4, 0x5005000
	s_nop 0
	v_addc_co_u32_e32 v13, vcc, 0, v57, vcc
	v_add_co_u32_e32 v20, vcc, s4, v56
	s_mov_b32 s4, 0x5007000
	s_nop 0
	v_addc_co_u32_e32 v21, vcc, 0, v57, vcc
	v_add_co_u32_e32 v32, vcc, s4, v56
	s_mov_b32 s4, 0x5009000
	s_nop 0
	v_addc_co_u32_e32 v33, vcc, 0, v57, vcc
	v_add_co_u32_e32 v40, vcc, s4, v56
	s_mov_b32 s4, 0x500b000
	s_nop 0
	v_addc_co_u32_e32 v41, vcc, 0, v57, vcc
	v_add_co_u32_e32 v48, vcc, s4, v56
	s_mov_b32 s4, 0x500d000
	s_nop 0
	v_addc_co_u32_e32 v49, vcc, 0, v57, vcc
	v_add_co_u32_e32 v58, vcc, s4, v56
	s_mov_b32 s4, 0x500f000
	s_nop 0
	v_addc_co_u32_e32 v59, vcc, 0, v57, vcc
	v_add_co_u32_e32 v64, vcc, s4, v56
	global_load_dwordx4 v[28:31], v[4:5], off offset:-4096 nt
	global_load_dwordx4 v[0:3], v[4:5], off nt
	v_addc_co_u32_e32 v65, vcc, 0, v57, vcc
	global_load_dwordx4 v[4:7], v[12:13], off offset:-4096 nt
	global_load_dwordx4 v[8:11], v[12:13], off nt
	s_nop 0
	global_load_dwordx4 v[12:15], v[20:21], off offset:-4096 nt
	global_load_dwordx4 v[16:19], v[20:21], off nt
	s_nop 0
	global_load_dwordx4 v[20:23], v[32:33], off offset:-4096 nt
	global_load_dwordx4 v[24:27], v[32:33], off nt
	s_nop 0
	global_load_dwordx4 v[32:35], v[40:41], off offset:-4096 nt
	global_load_dwordx4 v[36:39], v[40:41], off nt
	s_nop 0
	global_load_dwordx4 v[40:43], v[48:49], off offset:-4096 nt
	global_load_dwordx4 v[44:47], v[48:49], off nt
	s_nop 0
	global_load_dwordx4 v[48:51], v[58:59], off offset:-4096 nt
	global_load_dwordx4 v[52:55], v[58:59], off nt
	s_nop 0
	global_load_dwordx4 v[56:59], v[64:65], off offset:-4096 nt
	global_load_dwordx4 v[60:63], v[64:65], off nt
	s_lshl_b32 s13, s6, 5
	s_add_u32 s14, s10, 0x2900000
	v_readlane_b32 s6, v243, 0
	s_addc_u32 s15, s11, 0
	s_mov_b32 s8, s6
	s_lshl_b32 s4, s6, 5
	s_lshl_b32 s6, s94, 2
	s_add_i32 s4, s4, s6
	s_lshl_b32 s6, s38, 5
	s_sub_i32 s16, s4, s6
	s_lshl_b32 s4, s8, 3
	s_add_i32 s4, s94, s4
	s_lshl_b32 s6, s38, 3
	s_sub_i32 s4, s4, s6
	v_ashrrev_i32_e32 v133, 31, v132
	s_add_i32 s17, s4, 0x3c0
	s_movk_i32 s18, 0x2000
	s_movk_i32 s19, 0x4000
	s_movk_i32 s20, 0x6000
	s_mov_b32 s21, 0x8000
	s_mov_b32 s22, 0xa000
	s_mov_b32 s23, 0xb000
	s_mov_b32 s24, 0xc000
	s_mov_b32 s25, 0xc3e00000
	v_mov_b32_e32 v135, 0x43e00000
	v_readlane_b32 s7, v243, 1
	s_branch .LBB0_261

.LBB0_259:
	s_nop 1
	v_mul_f32_e32 v128, 0x42000000, v109
	v_mul_f32_e32 v129, 0x42000000, v69
	v_med3_f32 v131, v128, s25, v135
	v_med3_f32 v129, v129, s25, v135
	v_mov_b32_e32 v128, v137
	v_cvt_pk_fp8_f32 v128, v131, v129
	v_mul_f32_e32 v130, 0x42000000, v65
	v_mul_f32_e32 v129, 0x42000000, v77
	v_med3_f32 v130, v130, s25, v135
	v_med3_f32 v129, v129, s25, v135
	v_cvt_pk_fp8_f32 v128, v130, v129 op_sel:[0,0,1]
	v_mul_f32_e32 v129, 0x42000000, v73
	v_mul_f32_e32 v130, 0x42000000, v85
	v_med3_f32 v136, v129, s25, v135
	v_med3_f32 v130, v130, s25, v135
	v_mov_b32_e32 v129, v137
	v_cvt_pk_fp8_f32 v129, v136, v130
	v_mul_f32_e32 v131, 0x42000000, v81
	v_mul_f32_e32 v130, 0x42000000, v93
	v_med3_f32 v131, v131, s25, v135
	v_med3_f32 v130, v130, s25, v135
	v_cvt_pk_fp8_f32 v129, v131, v130 op_sel:[0,0,1]
	v_mul_f32_e32 v130, 0x42000000, v89
	v_mul_f32_e32 v131, 0x42000000, v101
	v_med3_f32 v143, v130, s25, v135
	v_med3_f32 v131, v131, s25, v135
	v_mov_b32_e32 v130, v137
	v_cvt_pk_fp8_f32 v130, v143, v131
	v_mul_f32_e32 v136, 0x42000000, v97
	v_mul_f32_e32 v131, 0x42000000, v105
	v_med3_f32 v136, v136, s25, v135
	v_med3_f32 v131, v131, s25, v135
	v_cvt_pk_fp8_f32 v130, v136, v131 op_sel:[0,0,1]
	v_mul_f32_e32 v131, 0x42000000, v113
	v_mul_f32_e32 v136, 0x42000000, v117
	v_med3_f32 v144, v131, s25, v135
	v_med3_f32 v136, v136, s25, v135
	v_mov_b32_e32 v131, v137
	v_cvt_pk_fp8_f32 v131, v144, v136
	v_mul_f32_e32 v143, 0x42000000, v121
	v_mul_f32_e32 v136, 0x42000000, v125
	v_med3_f32 v143, v143, s25, v135
	v_med3_f32 v136, v136, s25, v135
	v_cvt_pk_fp8_f32 v131, v143, v136 op_sel:[0,0,1]
	v_mul_f32_e32 v136, 0x42000000, v110
	v_mul_f32_e32 v143, 0x42000000, v70
	v_med3_f32 v136, v136, s25, v135
	v_med3_f32 v143, v143, s25, v135
	v_mov_b32_e32 v144, v137
	v_cvt_pk_fp8_f32 v144, v136, v143
	v_mul_f32_e32 v145, 0x42000000, v66
	v_mul_f32_e32 v136, 0x42000000, v78
	v_med3_f32 v143, v145, s25, v135
	v_med3_f32 v136, v136, s25, v135
	v_cvt_pk_fp8_f32 v144, v143, v136 op_sel:[0,0,1]
	v_mul_f32_e32 v136, 0x42000000, v74
	v_mul_f32_e32 v143, 0x42000000, v86
	v_med3_f32 v136, v136, s25, v135
	v_med3_f32 v143, v143, s25, v135
	v_mov_b32_e32 v145, v137
	v_cvt_pk_fp8_f32 v145, v136, v143
	v_mul_f32_e32 v146, 0x42000000, v82
	v_mul_f32_e32 v136, 0x42000000, v94
	v_med3_f32 v143, v146, s25, v135
	v_med3_f32 v136, v136, s25, v135
	v_cvt_pk_fp8_f32 v145, v143, v136 op_sel:[0,0,1]
	v_mul_f32_e32 v136, 0x42000000, v90
	v_mul_f32_e32 v143, 0x42000000, v102
	v_med3_f32 v136, v136, s25, v135
	v_med3_f32 v143, v143, s25, v135
	v_mov_b32_e32 v146, v137
	v_cvt_pk_fp8_f32 v146, v136, v143
	v_mul_f32_e32 v147, 0x42000000, v98
	v_mul_f32_e32 v136, 0x42000000, v106
	v_med3_f32 v143, v147, s25, v135
	v_med3_f32 v136, v136, s25, v135
	v_cvt_pk_fp8_f32 v146, v143, v136 op_sel:[0,0,1]
	v_mul_f32_e32 v136, 0x42000000, v114
	v_mul_f32_e32 v143, 0x42000000, v118
	v_med3_f32 v136, v136, s25, v135
	v_med3_f32 v143, v143, s25, v135
	v_mov_b32_e32 v147, v137
	v_cvt_pk_fp8_f32 v147, v136, v143
	v_mul_f32_e32 v148, 0x42000000, v122
	v_mul_f32_e32 v136, 0x42000000, v126
	v_med3_f32 v143, v148, s25, v135
	v_med3_f32 v136, v136, s25, v135
	v_cvt_pk_fp8_f32 v147, v143, v136 op_sel:[0,0,1]
	v_lshl_add_u64 v[148:149], v[140:141], 0, s[8:9]
	global_store_dwordx4 v[148:149], v[128:131], off
	s_addk_i32 s13, 0x5000
	s_addk_i32 s17, 0x280
	v_lshl_add_u64 v[128:129], v[140:141], 0, s[6:7]
	global_store_dwordx4 v[128:129], v[144:147], off
	v_mul_f32_e32 v128, 0x42000000, v111
	v_mul_f32_e32 v129, 0x42000000, v71
	v_med3_f32 v131, v128, s25, v135
	v_med3_f32 v129, v129, s25, v135
	v_mov_b32_e32 v128, v137
	v_cvt_pk_fp8_f32 v128, v131, v129
	v_mul_f32_e32 v130, 0x42000000, v67
	v_mul_f32_e32 v129, 0x42000000, v79
	v_med3_f32 v130, v130, s25, v135
	v_med3_f32 v129, v129, s25, v135
	v_cvt_pk_fp8_f32 v128, v130, v129 op_sel:[0,0,1]
	v_mul_f32_e32 v129, 0x42000000, v75
	v_mul_f32_e32 v130, 0x42000000, v87
	v_med3_f32 v136, v129, s25, v135
	v_med3_f32 v130, v130, s25, v135
	v_mov_b32_e32 v129, v137
	v_cvt_pk_fp8_f32 v129, v136, v130
	v_mul_f32_e32 v131, 0x42000000, v83
	v_mul_f32_e32 v130, 0x42000000, v95
	v_med3_f32 v131, v131, s25, v135
	v_med3_f32 v130, v130, s25, v135
	v_cvt_pk_fp8_f32 v129, v131, v130 op_sel:[0,0,1]
	v_mul_f32_e32 v130, 0x42000000, v91
	v_mul_f32_e32 v131, 0x42000000, v103
	v_med3_f32 v140, v130, s25, v135
	v_med3_f32 v131, v131, s25, v135
	v_mov_b32_e32 v130, v137
	v_cvt_pk_fp8_f32 v130, v140, v131
	v_mul_f32_e32 v136, 0x42000000, v99
	v_mul_f32_e32 v131, 0x42000000, v107
	v_med3_f32 v136, v136, s25, v135
	v_med3_f32 v131, v131, s25, v135
	v_cvt_pk_fp8_f32 v130, v136, v131 op_sel:[0,0,1]
	v_mul_f32_e32 v131, 0x42000000, v115
	v_mul_f32_e32 v136, 0x42000000, v119
	v_med3_f32 v141, v131, s25, v135
	v_med3_f32 v136, v136, s25, v135
	v_mov_b32_e32 v131, v137
	v_cvt_pk_fp8_f32 v131, v141, v136
	v_mul_f32_e32 v140, 0x42000000, v123
	v_mul_f32_e32 v136, 0x42000000, v127
	v_med3_f32 v140, v140, s25, v135
	v_med3_f32 v136, v136, s25, v135
	v_cvt_pk_fp8_f32 v131, v140, v136 op_sel:[0,0,1]
	v_or_b32_e32 v136, s4, v142
	v_lshlrev_b32_e32 v136, 10, v136
	v_lshl_add_u64 v[138:139], v[138:139], 0, v[136:137]
	s_cmpk_gt_i32 s26, 0x337f
	global_store_dwordx4 v[138:139], v[128:131], off
	s_cselect_b64 s[6:7], -1, 0

.LBB0_261:
	s_add_i32 s26, s17, 0xfffffd80
	s_add_i32 s27, s17, 0xfffffec0
	s_cmpk_lt_i32 s26, 0x34c0
	s_cselect_b64 s[6:7], -1, 0
	s_cmpk_gt_i32 s26, 0x34bf
	s_cbranch_scc1 .LBB0_263
	s_bitcmp0_b32 s27, 8
	s_cselect_b32 s4, s12, 0x108
	s_add_u32 s8, s0, s4
	s_addc_u32 s9, s1, 0
	s_load_dwordx2 s[8:9], s[8:9], 0x0
	s_lshr_b32 s4, s27, 9
	s_add_i32 s4, s4, 20
	s_lshl_b64 s[10:11], s[4:5], 22
	v_lshlrev_b32_e32 v136, 2, v134
	s_waitcnt lgkmcnt(0)
	s_add_u32 s8, s8, s10
	s_addc_u32 s9, s9, s11
	s_add_i32 s4, s16, 0xa00
	s_and_b32 s4, s4, 0x380
	v_add_u32_e32 v64, s4, v132
	v_ashrrev_i32_e32 v65, 31, v64
	s_and_b32 s10, s13, 0x3e0
	v_lshlrev_b64 v[64:65], 12, v[64:65]
	v_lshl_add_u64 v[64:65], s[8:9], 0, v[64:65]
	s_lshl_b32 s4, s10, 2
	v_lshl_add_u64 v[64:65], v[64:65], 0, s[4:5]
	v_lshl_add_u64 v[120:121], v[64:65], 0, v[136:137]
	v_add_co_u32_e32 v72, vcc, s18, v120
	s_nop 1
	v_addc_co_u32_e32 v73, vcc, 0, v121, vcc
	v_add_co_u32_e32 v80, vcc, s19, v120
	global_load_dwordx4 v[68:71], v[72:73], off offset:-4096 nt
	global_load_dwordx4 v[64:67], v[72:73], off nt
	v_addc_co_u32_e32 v81, vcc, 0, v121, vcc
	v_add_co_u32_e32 v88, vcc, s20, v120
	global_load_dwordx4 v[76:79], v[80:81], off offset:-4096 nt
	global_load_dwordx4 v[72:75], v[80:81], off nt
	v_addc_co_u32_e32 v89, vcc, 0, v121, vcc
	v_add_co_u32_e32 v96, vcc, s21, v120
	global_load_dwordx4 v[84:87], v[88:89], off offset:-4096 nt
	global_load_dwordx4 v[80:83], v[88:89], off nt
	v_addc_co_u32_e32 v97, vcc, 0, v121, vcc
	v_add_co_u32_e32 v104, vcc, s22, v120
	global_load_dwordx4 v[92:95], v[96:97], off offset:-4096 nt
	global_load_dwordx4 v[88:91], v[96:97], off nt
	v_addc_co_u32_e32 v105, vcc, 0, v121, vcc
	v_add_co_u32_e32 v112, vcc, s23, v120
	global_load_dwordx4 v[100:103], v[104:105], off offset:-4096 nt
	global_load_dwordx4 v[96:99], v[104:105], off nt
	v_addc_co_u32_e32 v113, vcc, 0, v121, vcc
	global_load_dwordx4 v[108:111], v[120:121], off nt
	global_load_dwordx4 v[104:107], v[112:113], off nt
	v_add_co_u32_e32 v112, vcc, 0xc000, v120
	s_nop 1
	v_addc_co_u32_e32 v113, vcc, 0, v121, vcc
	v_add_co_u32_e32 v116, vcc, 0xd000, v120
	s_nop 1
	v_addc_co_u32_e32 v117, vcc, 0, v121, vcc
	v_add_co_u32_e32 v122, vcc, 0xe000, v120
	global_load_dwordx4 v[112:115], v[112:113], off nt
	s_nop 0
	global_load_dwordx4 v[116:119], v[116:117], off nt
	v_addc_co_u32_e32 v123, vcc, 0, v121, vcc
	v_add_co_u32_e32 v124, vcc, 0xf000, v120
	s_nop 1
	v_addc_co_u32_e32 v125, vcc, 0, v121, vcc
	global_load_dwordx4 v[120:123], v[122:123], off nt
	s_nop 0
	global_load_dwordx4 v[124:127], v[124:125], off nt
.LBB0_263:
	s_waitcnt vmcnt(6)
	v_mul_f32_e32 v128, 0x42000000, v28
	s_waitcnt vmcnt(14)
	v_mul_f32_e32 v129, 0x42000000, v0
	v_med3_f32 v131, v128, s25, v135
	v_med3_f32 v129, v129, s25, v135
	v_mov_b32_e32 v128, v137
	v_cvt_pk_fp8_f32 v128, v131, v129
	s_waitcnt vmcnt(13)
	v_mul_f32_e32 v130, 0x42000000, v4
	s_waitcnt vmcnt(12)
	v_mul_f32_e32 v129, 0x42000000, v8
	v_med3_f32 v130, v130, s25, v135
	v_med3_f32 v129, v129, s25, v135
	v_cvt_pk_fp8_f32 v128, v130, v129 op_sel:[0,0,1]
	s_waitcnt vmcnt(11)
	v_mul_f32_e32 v129, 0x42000000, v12
	s_waitcnt vmcnt(10)
	v_mul_f32_e32 v130, 0x42000000, v16
	v_med3_f32 v136, v129, s25, v135
	v_med3_f32 v130, v130, s25, v135
	v_mov_b32_e32 v129, v137
	v_cvt_pk_fp8_f32 v129, v136, v130
	s_waitcnt vmcnt(9)
	v_mul_f32_e32 v131, 0x42000000, v20
	s_waitcnt vmcnt(8)
	v_mul_f32_e32 v130, 0x42000000, v24
	v_med3_f32 v131, v131, s25, v135
	v_med3_f32 v130, v130, s25, v135
	v_cvt_pk_fp8_f32 v129, v131, v130 op_sel:[0,0,1]
	s_waitcnt vmcnt(7)
	v_mul_f32_e32 v130, 0x42000000, v32
	s_waitcnt vmcnt(6)
	v_mul_f32_e32 v131, 0x42000000, v36
	v_med3_f32 v140, v130, s25, v135
	v_med3_f32 v131, v131, s25, v135
	v_mov_b32_e32 v130, v137
	v_cvt_pk_fp8_f32 v130, v140, v131
	s_waitcnt vmcnt(5)
	v_mul_f32_e32 v136, 0x42000000, v40
	s_waitcnt vmcnt(4)
	v_mul_f32_e32 v131, 0x42000000, v44
	s_lshr_b32 s4, s26, 9
	v_med3_f32 v136, v136, s25, v135
	v_med3_f32 v131, v131, s25, v135
	s_add_i32 s4, s4, 20
	v_cvt_pk_fp8_f32 v130, v136, v131 op_sel:[0,0,1]
	s_waitcnt vmcnt(3)
	v_mul_f32_e32 v131, 0x42000000, v48
	s_waitcnt vmcnt(2)
	v_mul_f32_e32 v136, 0x42000000, v52
	s_mul_hi_u32 s8, s4, 0x300000
	s_mul_i32 s4, s4, 0x300000
	v_med3_f32 v141, v131, s25, v135
	v_med3_f32 v136, v136, s25, v135
	v_mov_b32_e32 v131, v137
	s_add_u32 s4, s14, s4
	v_cvt_pk_fp8_f32 v131, v141, v136
	s_addc_u32 s9, s15, s8
	s_lshl_b32 s11, s26, 5
	s_lshl_b32 s28, s26, 6
	s_add_i32 s8, s16, 0x500
	s_and_b32 s28, s28, 0x700
	s_and_b32 s11, s11, 0x60
	s_waitcnt vmcnt(1)
	v_mul_f32_e32 v140, 0x42000000, v56
	s_waitcnt vmcnt(0)
	v_mul_f32_e32 v136, 0x42000000, v60
	s_and_b32 s10, s26, 0x100
	s_and_b32 s8, s8, 0x380
	s_or_b32 s11, s11, s28
	v_med3_f32 v140, v140, s25, v135
	v_med3_f32 v136, v136, s25, v135
	s_add_u32 s8, s4, s8
	v_cvt_pk_fp8_f32 v131, v140, v136 op_sel:[0,0,1]
	s_addc_u32 s9, s9, 0
	v_or_b32_e32 v142, s11, v134
	v_lshl_add_u64 v[138:139], s[8:9], 0, v[132:133]
	v_lshlrev_b32_e32 v136, 10, v142
	s_cmp_lg_u32 s10, 0
	v_lshl_add_u64 v[140:141], v[138:139], 0, v[136:137]
	s_mov_b64 s[8:9], -1
	s_cbranch_scc0 .LBB0_265
	v_add_co_u32_e32 v144, vcc, 0x20000, v140
	s_mov_b64 s[8:9], 0
	s_nop 0
	v_addc_co_u32_e32 v145, vcc, 0, v141, vcc
	global_store_dwordx4 v[144:145], v[128:131], off

.LBB0_268:
	s_nop 0
	v_mul_f32_e32 v128, 0x42000000, v29
	v_mul_f32_e32 v129, 0x42000000, v1
	v_med3_f32 v131, v128, s25, v135
	v_med3_f32 v129, v129, s25, v135
	v_mov_b32_e32 v128, v137
	v_cvt_pk_fp8_f32 v128, v131, v129
	v_mul_f32_e32 v130, 0x42000000, v5
	v_mul_f32_e32 v129, 0x42000000, v9
	v_med3_f32 v130, v130, s25, v135
	v_med3_f32 v129, v129, s25, v135
	v_cvt_pk_fp8_f32 v128, v130, v129 op_sel:[0,0,1]
	v_mul_f32_e32 v129, 0x42000000, v13
	v_mul_f32_e32 v130, 0x42000000, v17
	v_med3_f32 v143, v129, s25, v135
	v_med3_f32 v130, v130, s25, v135
	v_mov_b32_e32 v129, v137
	v_cvt_pk_fp8_f32 v129, v143, v130
	v_mul_f32_e32 v131, 0x42000000, v21
	v_mul_f32_e32 v130, 0x42000000, v25
	v_med3_f32 v131, v131, s25, v135
	v_med3_f32 v130, v130, s25, v135
	v_cvt_pk_fp8_f32 v129, v131, v130 op_sel:[0,0,1]
	v_mul_f32_e32 v130, 0x42000000, v33
	v_mul_f32_e32 v131, 0x42000000, v37
	v_med3_f32 v144, v130, s25, v135
	v_med3_f32 v131, v131, s25, v135
	v_mov_b32_e32 v130, v137
	v_cvt_pk_fp8_f32 v130, v144, v131
	v_mul_f32_e32 v143, 0x42000000, v41
	v_mul_f32_e32 v131, 0x42000000, v45
	v_med3_f32 v143, v143, s25, v135
	v_med3_f32 v131, v131, s25, v135
	v_cvt_pk_fp8_f32 v130, v143, v131 op_sel:[0,0,1]
	v_mul_f32_e32 v131, 0x42000000, v49
	v_mul_f32_e32 v143, 0x42000000, v53
	v_med3_f32 v145, v131, s25, v135
	v_med3_f32 v143, v143, s25, v135
	v_mov_b32_e32 v131, v137
	v_cvt_pk_fp8_f32 v131, v145, v143
	v_mul_f32_e32 v144, 0x42000000, v57
	v_mul_f32_e32 v143, 0x42000000, v61
	v_med3_f32 v144, v144, s25, v135
	v_med3_f32 v143, v143, s25, v135
	v_cvt_pk_fp8_f32 v131, v144, v143 op_sel:[0,0,1]
	v_mul_f32_e32 v143, 0x42000000, v30
	v_mul_f32_e32 v144, 0x42000000, v2
	v_med3_f32 v143, v143, s25, v135
	v_med3_f32 v146, v144, s25, v135
	v_mov_b32_e32 v144, v137
	v_cvt_pk_fp8_f32 v144, v143, v146
	v_mul_f32_e32 v145, 0x42000000, v6
	v_mul_f32_e32 v143, 0x42000000, v10
	v_med3_f32 v145, v145, s25, v135
	v_med3_f32 v143, v143, s25, v135
	v_cvt_pk_fp8_f32 v144, v145, v143 op_sel:[0,0,1]
	v_mul_f32_e32 v143, 0x42000000, v14
	v_mul_f32_e32 v145, 0x42000000, v18
	v_med3_f32 v143, v143, s25, v135
	v_med3_f32 v147, v145, s25, v135
	v_mov_b32_e32 v145, v137
	v_cvt_pk_fp8_f32 v145, v143, v147
	v_mul_f32_e32 v146, 0x42000000, v22
	v_mul_f32_e32 v143, 0x42000000, v26
	v_med3_f32 v146, v146, s25, v135
	v_med3_f32 v143, v143, s25, v135
	v_cvt_pk_fp8_f32 v145, v146, v143 op_sel:[0,0,1]
	v_mul_f32_e32 v143, 0x42000000, v34
	v_mul_f32_e32 v146, 0x42000000, v38
	v_med3_f32 v143, v143, s25, v135
	v_med3_f32 v148, v146, s25, v135
	v_mov_b32_e32 v146, v137
	v_cvt_pk_fp8_f32 v146, v143, v148
	v_mul_f32_e32 v147, 0x42000000, v42
	v_mul_f32_e32 v143, 0x42000000, v46
	v_med3_f32 v147, v147, s25, v135
	v_med3_f32 v143, v143, s25, v135
	v_cvt_pk_fp8_f32 v146, v147, v143 op_sel:[0,0,1]
	v_mul_f32_e32 v143, 0x42000000, v50
	v_mul_f32_e32 v147, 0x42000000, v54
	v_med3_f32 v143, v143, s25, v135
	v_med3_f32 v149, v147, s25, v135
	v_mov_b32_e32 v147, v137
	v_cvt_pk_fp8_f32 v147, v143, v149
	v_mul_f32_e32 v148, 0x42000000, v58
	v_mul_f32_e32 v143, 0x42000000, v62
	v_med3_f32 v148, v148, s25, v135
	v_med3_f32 v143, v143, s25, v135
	v_cvt_pk_fp8_f32 v147, v148, v143 op_sel:[0,0,1]
	v_lshl_add_u64 v[148:149], v[140:141], 0, s[10:11]
	global_store_dwordx4 v[148:149], v[128:131], off
	s_andn2_b64 vcc, exec, s[6:7]
	s_mov_b64 s[6:7], -1
	v_lshl_add_u64 v[128:129], v[140:141], 0, s[8:9]
	global_store_dwordx4 v[128:129], v[144:147], off
	v_mul_f32_e32 v128, 0x42000000, v31
	v_mul_f32_e32 v129, 0x42000000, v3
	v_med3_f32 v131, v128, s25, v135
	v_med3_f32 v129, v129, s25, v135
	v_mov_b32_e32 v128, v137
	v_cvt_pk_fp8_f32 v128, v131, v129
	v_mul_f32_e32 v130, 0x42000000, v7
	v_mul_f32_e32 v129, 0x42000000, v11
	v_med3_f32 v130, v130, s25, v135
	v_med3_f32 v129, v129, s25, v135
	v_cvt_pk_fp8_f32 v128, v130, v129 op_sel:[0,0,1]
	v_mul_f32_e32 v129, 0x42000000, v15
	v_mul_f32_e32 v130, 0x42000000, v19
	v_med3_f32 v140, v129, s25, v135
	v_med3_f32 v130, v130, s25, v135
	v_mov_b32_e32 v129, v137
	v_cvt_pk_fp8_f32 v129, v140, v130
	v_mul_f32_e32 v131, 0x42000000, v23
	v_mul_f32_e32 v130, 0x42000000, v27
	v_med3_f32 v131, v131, s25, v135
	v_med3_f32 v130, v130, s25, v135
	v_cvt_pk_fp8_f32 v129, v131, v130 op_sel:[0,0,1]
	v_mul_f32_e32 v130, 0x42000000, v35
	v_mul_f32_e32 v131, 0x42000000, v39
	v_med3_f32 v141, v130, s25, v135
	v_med3_f32 v131, v131, s25, v135
	v_mov_b32_e32 v130, v137
	v_cvt_pk_fp8_f32 v130, v141, v131
	v_mul_f32_e32 v140, 0x42000000, v43
	v_mul_f32_e32 v131, 0x42000000, v47
	v_med3_f32 v140, v140, s25, v135
	v_med3_f32 v131, v131, s25, v135
	v_cvt_pk_fp8_f32 v130, v140, v131 op_sel:[0,0,1]
	v_mul_f32_e32 v131, 0x42000000, v51
	v_mul_f32_e32 v140, 0x42000000, v55
	v_med3_f32 v143, v131, s25, v135
	v_med3_f32 v140, v140, s25, v135
	v_mov_b32_e32 v131, v137
	v_cvt_pk_fp8_f32 v131, v143, v140
	v_mul_f32_e32 v141, 0x42000000, v59
	v_mul_f32_e32 v140, 0x42000000, v63
	v_med3_f32 v141, v141, s25, v135
	v_med3_f32 v140, v140, s25, v135
	v_cvt_pk_fp8_f32 v131, v141, v140 op_sel:[0,0,1]
	v_or_b32_e32 v140, s4, v142
	v_lshlrev_b32_e32 v140, 10, v140
	v_mov_b32_e32 v141, v137
	v_lshl_add_u64 v[138:139], v[138:139], 0, v[140:141]
	global_store_dwordx4 v[138:139], v[128:131], off
	s_cbranch_vccnz .LBB0_260
	s_cmpk_gt_i32 s26, 0x337f
	s_cbranch_scc1 .LBB0_271
	s_bitcmp0_b32 s17, 8
	s_cselect_b32 s4, s12, 0x108
	s_add_u32 s6, s0, s4
	s_addc_u32 s7, s1, 0
	s_load_dwordx2 s[6:7], s[6:7], 0x0
	s_lshr_b32 s4, s17, 9
	s_add_i32 s4, s4, 20
	s_lshl_b64 s[8:9], s[4:5], 22
	v_lshlrev_b32_e32 v2, 2, v134
	s_waitcnt lgkmcnt(0)
	s_add_u32 s6, s6, s8
	s_addc_u32 s7, s7, s9
	s_add_i32 s4, s16, 0xf00
	s_and_b32 s4, s4, 0x380
	v_add_u32_e32 v0, s4, v132
	v_ashrrev_i32_e32 v1, 31, v0
	s_and_b32 s8, s13, 0x3e0
	v_lshlrev_b64 v[0:1], 12, v[0:1]
	v_lshl_add_u64 v[0:1], s[6:7], 0, v[0:1]
	s_lshl_b32 s4, s8, 2
	v_lshl_add_u64 v[0:1], v[0:1], 0, s[4:5]
	v_mov_b32_e32 v3, v137
	v_lshl_add_u64 v[56:57], v[0:1], 0, v[2:3]
	v_add_co_u32_e32 v8, vcc, s18, v56
	s_nop 1
	v_addc_co_u32_e32 v9, vcc, 0, v57, vcc
	v_add_co_u32_e32 v16, vcc, s19, v56
	global_load_dwordx4 v[0:3], v[8:9], off offset:-4096 nt
	global_load_dwordx4 v[4:7], v[8:9], off nt
	v_addc_co_u32_e32 v17, vcc, 0, v57, vcc
	v_add_co_u32_e32 v24, vcc, s20, v56
	global_load_dwordx4 v[8:11], v[16:17], off offset:-4096 nt
	global_load_dwordx4 v[12:15], v[16:17], off nt
	v_addc_co_u32_e32 v25, vcc, 0, v57, vcc
	v_add_co_u32_e32 v28, vcc, s21, v56
	global_load_dwordx4 v[16:19], v[24:25], off offset:-4096 nt
	global_load_dwordx4 v[20:23], v[24:25], off nt
	v_addc_co_u32_e32 v29, vcc, 0, v57, vcc
	global_load_dwordx4 v[24:27], v[28:29], off offset:-4096 nt
	global_load_dwordx4 v[32:35], v[28:29], off nt
	v_add_co_u32_e32 v28, vcc, s22, v56
	s_nop 1
	v_addc_co_u32_e32 v29, vcc, 0, v57, vcc
	global_load_dwordx4 v[36:39], v[28:29], off offset:-4096 nt
	global_load_dwordx4 v[40:43], v[28:29], off nt
	v_add_co_u32_e32 v28, vcc, s24, v56
	s_nop 1
	v_addc_co_u32_e32 v29, vcc, 0, v57, vcc
	v_add_co_u32_e32 v52, vcc, 0xd000, v56
	global_load_dwordx4 v[44:47], v[28:29], off offset:-4096 nt
	global_load_dwordx4 v[48:51], v[28:29], off nt
	v_addc_co_u32_e32 v53, vcc, 0, v57, vcc
	v_add_co_u32_e32 v58, vcc, 0xe000, v56
	global_load_dwordx4 v[28:31], v[56:57], off nt
	s_nop 0
	global_load_dwordx4 v[52:55], v[52:53], off nt
	v_addc_co_u32_e32 v59, vcc, 0, v57, vcc
	v_add_co_u32_e32 v60, vcc, 0xf000, v56
	s_nop 1
	v_addc_co_u32_e32 v61, vcc, 0, v57, vcc
	global_load_dwordx4 v[56:59], v[58:59], off nt
	s_nop 0
	global_load_dwordx4 v[60:63], v[60:61], off nt
.LBB0_271:
	v_mul_f32_e32 v128, 0x42000000, v108
	v_mul_f32_e32 v129, 0x42000000, v68
	v_med3_f32 v131, v128, s25, v135
	v_med3_f32 v129, v129, s25, v135
	v_mov_b32_e32 v128, v137
	v_cvt_pk_fp8_f32 v128, v131, v129
	v_mul_f32_e32 v130, 0x42000000, v64
	v_mul_f32_e32 v129, 0x42000000, v76
	v_med3_f32 v130, v130, s25, v135
	v_med3_f32 v129, v129, s25, v135
	v_cvt_pk_fp8_f32 v128, v130, v129 op_sel:[0,0,1]
	v_mul_f32_e32 v129, 0x42000000, v72
	v_mul_f32_e32 v130, 0x42000000, v84
	v_med3_f32 v138, v129, s25, v135
	v_med3_f32 v130, v130, s25, v135
	v_mov_b32_e32 v129, v137
	v_cvt_pk_fp8_f32 v129, v138, v130
	v_mul_f32_e32 v131, 0x42000000, v80
	v_mul_f32_e32 v130, 0x42000000, v92
	v_med3_f32 v131, v131, s25, v135
	v_med3_f32 v130, v130, s25, v135
	v_cvt_pk_fp8_f32 v129, v131, v130 op_sel:[0,0,1]
	v_mul_f32_e32 v130, 0x42000000, v88
	v_mul_f32_e32 v131, 0x42000000, v100
	v_med3_f32 v139, v130, s25, v135
	v_med3_f32 v131, v131, s25, v135
	v_mov_b32_e32 v130, v137
	v_cvt_pk_fp8_f32 v130, v139, v131
	v_mul_f32_e32 v138, 0x42000000, v96
	v_mul_f32_e32 v131, 0x42000000, v104
	v_med3_f32 v138, v138, s25, v135
	v_med3_f32 v131, v131, s25, v135
	s_lshr_b32 s4, s27, 9
	v_cvt_pk_fp8_f32 v130, v138, v131 op_sel:[0,0,1]
	v_mul_f32_e32 v131, 0x42000000, v112
	v_mul_f32_e32 v138, 0x42000000, v116
	s_add_i32 s4, s4, 20
	v_med3_f32 v140, v131, s25, v135
	v_med3_f32 v138, v138, s25, v135
	v_mov_b32_e32 v131, v137
	s_mul_hi_u32 s6, s4, 0x300000
	s_mul_i32 s4, s4, 0x300000
	v_cvt_pk_fp8_f32 v131, v140, v138
	s_add_u32 s4, s14, s4
	s_addc_u32 s7, s15, s6
	s_addk_i32 s16, 0xa00
	v_mul_f32_e32 v139, 0x42000000, v120
	v_mul_f32_e32 v138, 0x42000000, v124
	s_and_b32 s8, s27, 0x100
	s_and_b32 s6, s16, 0x380
	v_med3_f32 v139, v139, s25, v135
	v_med3_f32 v138, v138, s25, v135
	s_add_u32 s6, s4, s6
	v_cvt_pk_fp8_f32 v131, v139, v138 op_sel:[0,0,1]
	s_addc_u32 s7, s7, 0
	v_lshl_add_u64 v[138:139], s[6:7], 0, v[132:133]
	s_cmp_lg_u32 s8, 0
	v_lshl_add_u64 v[140:141], v[138:139], 0, v[136:137]
	s_mov_b64 s[6:7], -1
	s_cbranch_scc0 .LBB0_273
	v_add_co_u32_e32 v144, vcc, 0x20000, v140
	s_mov_b64 s[6:7], 0
	s_nop 0
	v_addc_co_u32_e32 v145, vcc, 0, v141, vcc
	global_store_dwordx4 v[144:145], v[128:131], off

.LBB0_462:
	s_load_dwordx4 s[0:3], s[8:9], 0x138
	s_waitcnt lgkmcnt(0)
	s_mov_b64 s[4:5], s[0:1]
	s_cmp_lt_i32 s4, 5
	s_cselect_b64 s[0:1], -1, 0
	s_cmp_gt_i32 s5, 4
	s_cselect_b64 s[2:3], -1, 0
	s_and_b64 s[0:1], s[0:1], s[2:3]
	s_andn2_b64 vcc, exec, s[0:1]
	s_cbranch_vccnz .LBB0_559
	s_mov_b64 s[0:1], s[8:9]
	v_mbcnt_lo_u32_b32 v156, -1, 0
	v_mbcnt_hi_u32_b32 v156, -1, v156
	s_load_dword s56, s[8:9], 0x148
	s_add_u32 s4, s8, 0x148
	v_readlane_b32 s2, v243, 0
	s_addc_u32 s5, s9, 0
	v_readlane_b32 s3, v243, 1
	s_waitcnt lgkmcnt(0)
	s_sub_i32 s57, s56, 64
	s_cmp_lt_i32 s2, s57
	s_mov_b64 s[2:3], -1
	s_cbranch_scc1 .LBB0_485
	v_readlane_b32 s2, v243, 0
	s_sub_i32 s2, s2, s57
	s_lshl_b32 s6, s2, 3
	s_add_i32 s6, s6, s94
	s_cmpk_gt_u32 s6, 0x23ff
	v_readlane_b32 s3, v243, 1
	s_cbranch_scc1 .LBB0_484
	s_bitcmp0_b32 s6, 8
	s_movk_i32 s16, 0xf8
	s_cselect_b32 s17, s16, 0x108
	s_add_u32 s2, s0, s17
	s_addc_u32 s3, s1, 0
	s_load_dwordx2 s[8:9], s[2:3], 0x0
	s_load_dwordx2 s[10:11], s[0:1], 0x130
	s_lshl_b32 s2, s6, 13
	s_and_b32 s2, s2, 0x3c00000
	s_waitcnt vmcnt(0)
	v_lshlrev_b32_e32 v0, 1, v156
	s_waitcnt lgkmcnt(0)
	s_add_u32 s8, s8, s2
	s_addc_u32 s9, s9, 0
	s_lshl_b32 s18, s6, 2
	s_and_b32 s2, s18, 0x380
	v_and_b32_e32 v132, -16, v0
	v_add_u32_e32 v0, s2, v132
	v_ashrrev_i32_e32 v1, 31, v0
	v_lshlrev_b64 v[0:1], 12, v[0:1]
	s_lshl_b32 s2, s6, 7
	v_lshlrev_b32_e32 v2, 2, v156
	s_mov_b32 s3, 0
	v_lshl_add_u64 v[0:1], s[8:9], 0, v[0:1]
	s_and_b32 s2, s2, 0xf80
	v_and_b32_e32 v134, 28, v2
	v_lshl_add_u64 v[0:1], v[0:1], 0, s[2:3]
	v_mov_b32_e32 v137, 0
	v_lshlrev_b32_e32 v136, 2, v134
	v_lshl_add_u64 v[56:57], v[0:1], 0, v[136:137]
	s_mov_b32 s2, 0x801000
	v_add_co_u32_e32 v4, vcc, s2, v56
	s_mov_b32 s2, 0x803000
	s_nop 0
	v_addc_co_u32_e32 v5, vcc, 0, v57, vcc
	v_add_co_u32_e32 v12, vcc, s2, v56
	s_mov_b32 s2, 0x805000
	s_nop 0
	v_addc_co_u32_e32 v13, vcc, 0, v57, vcc
	v_add_co_u32_e32 v20, vcc, s2, v56
	s_mov_b32 s2, 0x807000
	s_nop 0
	v_addc_co_u32_e32 v21, vcc, 0, v57, vcc
	v_add_co_u32_e32 v32, vcc, s2, v56
	s_mov_b32 s2, 0x809000
	s_nop 0
	v_addc_co_u32_e32 v33, vcc, 0, v57, vcc
	v_add_co_u32_e32 v40, vcc, s2, v56
	s_mov_b32 s2, 0x80b000
	s_nop 0
	v_addc_co_u32_e32 v41, vcc, 0, v57, vcc
	v_add_co_u32_e32 v48, vcc, s2, v56
	s_mov_b32 s2, 0x80d000
	s_nop 0
	v_addc_co_u32_e32 v49, vcc, 0, v57, vcc
	v_add_co_u32_e32 v58, vcc, s2, v56
	s_mov_b32 s2, 0x80f000
	s_nop 0
	v_addc_co_u32_e32 v59, vcc, 0, v57, vcc
	v_add_co_u32_e32 v64, vcc, s2, v56
	global_load_dwordx4 v[28:31], v[4:5], off offset:-4096 nt
	global_load_dwordx4 v[0:3], v[4:5], off nt
	v_addc_co_u32_e32 v65, vcc, 0, v57, vcc
	global_load_dwordx4 v[4:7], v[12:13], off offset:-4096 nt
	global_load_dwordx4 v[8:11], v[12:13], off nt
	s_nop 0
	global_load_dwordx4 v[12:15], v[20:21], off offset:-4096 nt
	global_load_dwordx4 v[16:19], v[20:21], off nt
	s_nop 0
	global_load_dwordx4 v[20:23], v[32:33], off offset:-4096 nt
	global_load_dwordx4 v[24:27], v[32:33], off nt
	s_nop 0
	global_load_dwordx4 v[32:35], v[40:41], off offset:-4096 nt
	global_load_dwordx4 v[36:39], v[40:41], off nt
	s_nop 0
	global_load_dwordx4 v[40:43], v[48:49], off offset:-4096 nt
	global_load_dwordx4 v[44:47], v[48:49], off nt
	s_nop 0
	global_load_dwordx4 v[48:51], v[58:59], off offset:-4096 nt
	global_load_dwordx4 v[52:55], v[58:59], off nt
	s_nop 0
	global_load_dwordx4 v[56:59], v[64:65], off offset:-4096 nt
	global_load_dwordx4 v[60:63], v[64:65], off nt
	s_lshl_b32 s19, s6, 5
	s_add_u32 s20, s10, 0x2900000
	v_readlane_b32 s8, v243, 0
	s_addc_u32 s21, s11, 0
	s_lshl_b32 s2, s8, 3
	s_add_i32 s2, s2, s94
	s_lshl_b32 s7, s56, 3
	s_sub_i32 s2, s2, s7
	s_lshl_b32 s7, s2, 2
	s_lshr_b32 s6, s6, 9
	s_and_b32 s22, s7, 0x380
	s_add_i32 s23, s2, 0x600
	s_mul_hi_u32 s7, s6, 0x300000
	s_mul_i32 s6, s6, 0x300000
	s_add_u32 s6, s10, s6
	v_ashrrev_i32_e32 v133, 31, v132
	s_addc_u32 s7, s11, s7
	v_lshl_add_u64 v[64:65], s[6:7], 0, v[132:133]
	s_mov_b64 s[6:7], 0x2f00000
	v_lshl_add_u64 v[138:139], v[64:65], 0, s[6:7]
	v_readlane_b32 s6, v243, 6
	s_lshl_b32 s2, s2, 6
	s_lshr_b32 s6, s6, 1
	s_and_b32 s2, s2, 0x700
	s_and_b32 s6, s6, 0x60
	s_or_b32 s2, s2, s6
	v_or_b32_e32 v64, s2, v134
	v_lshlrev_b32_e32 v140, 10, v64
	v_mov_b32_e32 v141, v137
	s_movk_i32 s24, 0x2000
	s_movk_i32 s25, 0x4000
	s_movk_i32 s26, 0x6000
	s_mov_b32 s27, 0x8000
	s_mov_b32 s28, 0xa000
	s_mov_b32 s29, 0xb000
	s_mov_b32 s30, 0xc000
	s_mov_b32 s31, 0xc3e00000
	s_mov_b64 s[6:7], 0x600000
	v_mov_b32_e32 v135, 0x43e00000
	v_readlane_b32 s9, v243, 1
	s_branch .LBB0_468
.LBB0_466:
	v_mul_f32_e32 v128, 0x42000000, v111
	v_mul_f32_e32 v129, 0x42000000, v71
	v_med3_f32 v131, v128, s31, v135
	v_med3_f32 v129, v129, s31, v135
	v_mov_b32_e32 v128, v137
	v_cvt_pk_fp8_f32 v128, v131, v129
	v_mul_f32_e32 v130, 0x42000000, v67
	v_mul_f32_e32 v129, 0x42000000, v79
	v_med3_f32 v130, v130, s31, v135
	v_med3_f32 v129, v129, s31, v135
	v_cvt_pk_fp8_f32 v128, v130, v129 op_sel:[0,0,1]
	v_mul_f32_e32 v129, 0x42000000, v75
	v_mul_f32_e32 v130, 0x42000000, v87
	v_med3_f32 v136, v129, s31, v135
	v_med3_f32 v130, v130, s31, v135
	v_mov_b32_e32 v129, v137
	v_cvt_pk_fp8_f32 v129, v136, v130
	v_mul_f32_e32 v131, 0x42000000, v83
	v_mul_f32_e32 v130, 0x42000000, v95
	v_med3_f32 v131, v131, s31, v135
	v_med3_f32 v130, v130, s31, v135
	v_cvt_pk_fp8_f32 v129, v131, v130 op_sel:[0,0,1]
	v_mul_f32_e32 v130, 0x42000000, v91
	v_mul_f32_e32 v131, 0x42000000, v103
	v_med3_f32 v142, v130, s31, v135
	v_med3_f32 v131, v131, s31, v135
	v_mov_b32_e32 v130, v137
	v_cvt_pk_fp8_f32 v130, v142, v131
	v_mul_f32_e32 v136, 0x42000000, v99
	v_mul_f32_e32 v131, 0x42000000, v107
	v_med3_f32 v136, v136, s31, v135
	v_med3_f32 v131, v131, s31, v135
	v_cvt_pk_fp8_f32 v130, v136, v131 op_sel:[0,0,1]
	v_mul_f32_e32 v131, 0x42000000, v115
	v_mul_f32_e32 v136, 0x42000000, v119
	v_med3_f32 v143, v131, s31, v135
	v_med3_f32 v136, v136, s31, v135
	v_mov_b32_e32 v131, v137
	v_cvt_pk_fp8_f32 v131, v143, v136
	v_mul_f32_e32 v142, 0x42000000, v123
	v_mul_f32_e32 v136, 0x42000000, v127
	v_med3_f32 v142, v142, s31, v135
	v_med3_f32 v136, v136, s31, v135
	v_cvt_pk_fp8_f32 v131, v142, v136 op_sel:[0,0,1]
	v_or_b32_e32 v136, s8, v144
	s_add_u32 s8, s2, s22
	s_addc_u32 s9, s12, 0
	s_addk_i32 s18, 0x1000
	s_add_i32 s19, s19, 0x8000
	s_addk_i32 s23, 0x400
	v_lshl_add_u64 v[142:143], s[8:9], 0, v[132:133]
	v_lshlrev_b32_e32 v136, 10, v136
	s_cmpk_gt_i32 s34, 0x1fff
	v_lshl_add_u64 v[142:143], v[142:143], 0, v[136:137]
	v_lshl_add_u64 v[138:139], v[138:139], 0, s[6:7]
	s_cselect_b64 s[10:11], -1, 0
	global_store_dwordx4 v[142:143], v[128:131], off

.LBB0_468:
	s_add_i32 s34, s23, 0xfffffc00
	s_cmpk_lt_i32 s34, 0x2200
	s_cselect_b64 s[10:11], -1, 0
	s_mov_b64 s[8:9], -1
	s_and_b64 vcc, exec, s[10:11]
	s_cbranch_vccnz .LBB0_470
	s_and_b32 s2, s18, 0x380
	s_mov_b64 s[8:9], 0

.LBB0_477:
	s_nop 0
	v_mul_f32_e32 v128, 0x42000000, v29
	v_mul_f32_e32 v129, 0x42000000, v1
	v_med3_f32 v131, v128, s31, v135
	v_med3_f32 v129, v129, s31, v135
	v_mov_b32_e32 v128, v137
	v_cvt_pk_fp8_f32 v128, v131, v129
	v_mul_f32_e32 v130, 0x42000000, v5
	v_mul_f32_e32 v129, 0x42000000, v9
	v_med3_f32 v130, v130, s31, v135
	v_med3_f32 v129, v129, s31, v135
	v_cvt_pk_fp8_f32 v128, v130, v129 op_sel:[0,0,1]
	v_mul_f32_e32 v129, 0x42000000, v13
	v_mul_f32_e32 v130, 0x42000000, v17
	v_med3_f32 v136, v129, s31, v135
	v_med3_f32 v130, v130, s31, v135
	v_mov_b32_e32 v129, v137
	v_cvt_pk_fp8_f32 v129, v136, v130
	v_mul_f32_e32 v131, 0x42000000, v21
	v_mul_f32_e32 v130, 0x42000000, v25
	v_med3_f32 v131, v131, s31, v135
	v_med3_f32 v130, v130, s31, v135
	v_cvt_pk_fp8_f32 v129, v131, v130 op_sel:[0,0,1]
	v_mul_f32_e32 v130, 0x42000000, v33
	v_mul_f32_e32 v131, 0x42000000, v37
	v_med3_f32 v145, v130, s31, v135
	v_med3_f32 v131, v131, s31, v135
	v_mov_b32_e32 v130, v137
	v_cvt_pk_fp8_f32 v130, v145, v131
	v_mul_f32_e32 v136, 0x42000000, v41
	v_mul_f32_e32 v131, 0x42000000, v45
	v_med3_f32 v136, v136, s31, v135
	v_med3_f32 v131, v131, s31, v135
	v_cvt_pk_fp8_f32 v130, v136, v131 op_sel:[0,0,1]
	v_mul_f32_e32 v131, 0x42000000, v49
	v_mul_f32_e32 v136, 0x42000000, v53
	v_med3_f32 v146, v131, s31, v135
	v_med3_f32 v136, v136, s31, v135
	v_mov_b32_e32 v131, v137
	v_cvt_pk_fp8_f32 v131, v146, v136
	s_lshl_b32 s37, s34, 5
	s_lshl_b32 s38, s34, 6
	v_mul_f32_e32 v145, 0x42000000, v57
	v_mul_f32_e32 v136, 0x42000000, v61
	s_and_b32 s38, s38, 0x700
	s_and_b32 s37, s37, 0x60
	v_med3_f32 v145, v145, s31, v135
	v_med3_f32 v136, v136, s31, v135
	s_or_b32 s37, s37, s38
	v_cvt_pk_fp8_f32 v131, v145, v136 op_sel:[0,0,1]
	s_add_u32 s14, s14, s2
	s_addc_u32 s15, s15, 0
	v_lshl_add_u64 v[146:147], v[142:143], 0, s[14:15]
	global_store_dwordx4 v[146:147], v[128:131], off
	s_add_u32 s12, s12, s2
	s_addc_u32 s13, s13, 0
	v_mul_f32_e32 v128, 0x42000000, v30
	v_mul_f32_e32 v129, 0x42000000, v2
	v_med3_f32 v131, v128, s31, v135
	v_med3_f32 v129, v129, s31, v135
	v_mov_b32_e32 v128, v137
	v_cvt_pk_fp8_f32 v128, v131, v129
	v_mul_f32_e32 v130, 0x42000000, v6
	v_mul_f32_e32 v129, 0x42000000, v10
	v_med3_f32 v130, v130, s31, v135
	v_med3_f32 v129, v129, s31, v135
	v_cvt_pk_fp8_f32 v128, v130, v129 op_sel:[0,0,1]
	v_mul_f32_e32 v129, 0x42000000, v14
	v_mul_f32_e32 v130, 0x42000000, v18
	v_med3_f32 v136, v129, s31, v135
	v_med3_f32 v130, v130, s31, v135
	v_mov_b32_e32 v129, v137
	v_cvt_pk_fp8_f32 v129, v136, v130
	v_mul_f32_e32 v131, 0x42000000, v22
	v_mul_f32_e32 v130, 0x42000000, v26
	v_med3_f32 v131, v131, s31, v135
	v_med3_f32 v130, v130, s31, v135
	v_cvt_pk_fp8_f32 v129, v131, v130 op_sel:[0,0,1]
	v_mul_f32_e32 v130, 0x42000000, v34
	v_mul_f32_e32 v131, 0x42000000, v38
	v_med3_f32 v145, v130, s31, v135
	v_med3_f32 v131, v131, s31, v135
	v_mov_b32_e32 v130, v137
	v_cvt_pk_fp8_f32 v130, v145, v131
	v_mul_f32_e32 v136, 0x42000000, v42
	v_mul_f32_e32 v131, 0x42000000, v46
	v_med3_f32 v136, v136, s31, v135
	v_med3_f32 v131, v131, s31, v135
	v_cvt_pk_fp8_f32 v130, v136, v131 op_sel:[0,0,1]
	v_mul_f32_e32 v131, 0x42000000, v50
	v_mul_f32_e32 v136, 0x42000000, v54
	v_med3_f32 v146, v131, s31, v135
	v_med3_f32 v136, v136, s31, v135
	v_mov_b32_e32 v131, v137
	v_cvt_pk_fp8_f32 v131, v146, v136
	v_mul_f32_e32 v145, 0x42000000, v58
	v_mul_f32_e32 v136, 0x42000000, v62
	v_med3_f32 v145, v145, s31, v135
	v_med3_f32 v136, v136, s31, v135
	v_cvt_pk_fp8_f32 v131, v145, v136 op_sel:[0,0,1]
	v_lshl_add_u64 v[142:143], v[142:143], 0, s[12:13]
	v_or_b32_e32 v144, s37, v134
	s_andn2_b64 vcc, exec, s[10:11]
	global_store_dwordx4 v[142:143], v[128:131], off
	s_mov_b64 s[10:11], -1
	s_nop 0
	v_mul_f32_e32 v128, 0x42000000, v31
	v_mul_f32_e32 v129, 0x42000000, v3
	v_med3_f32 v131, v128, s31, v135
	v_med3_f32 v129, v129, s31, v135
	v_mov_b32_e32 v128, v137
	v_cvt_pk_fp8_f32 v128, v131, v129
	v_mul_f32_e32 v130, 0x42000000, v7
	v_mul_f32_e32 v129, 0x42000000, v11
	v_med3_f32 v130, v130, s31, v135
	v_med3_f32 v129, v129, s31, v135
	v_cvt_pk_fp8_f32 v128, v130, v129 op_sel:[0,0,1]
	v_mul_f32_e32 v129, 0x42000000, v15
	v_mul_f32_e32 v130, 0x42000000, v19
	v_med3_f32 v136, v129, s31, v135
	v_med3_f32 v130, v130, s31, v135
	v_mov_b32_e32 v129, v137
	v_cvt_pk_fp8_f32 v129, v136, v130
	v_mul_f32_e32 v131, 0x42000000, v23
	v_mul_f32_e32 v130, 0x42000000, v27
	v_med3_f32 v131, v131, s31, v135
	v_med3_f32 v130, v130, s31, v135
	v_cvt_pk_fp8_f32 v129, v131, v130 op_sel:[0,0,1]
	v_mul_f32_e32 v130, 0x42000000, v35
	v_mul_f32_e32 v131, 0x42000000, v39
	v_med3_f32 v142, v130, s31, v135
	v_med3_f32 v131, v131, s31, v135
	v_mov_b32_e32 v130, v137
	v_cvt_pk_fp8_f32 v130, v142, v131
	v_mul_f32_e32 v136, 0x42000000, v43
	v_mul_f32_e32 v131, 0x42000000, v47
	v_med3_f32 v136, v136, s31, v135
	v_med3_f32 v131, v131, s31, v135
	v_cvt_pk_fp8_f32 v130, v136, v131 op_sel:[0,0,1]
	v_mul_f32_e32 v131, 0x42000000, v51
	v_mul_f32_e32 v136, 0x42000000, v55
	v_med3_f32 v143, v131, s31, v135
	v_med3_f32 v136, v136, s31, v135
	v_mov_b32_e32 v131, v137
	v_cvt_pk_fp8_f32 v131, v143, v136
	v_mul_f32_e32 v142, 0x42000000, v59
	v_mul_f32_e32 v136, 0x42000000, v63
	v_med3_f32 v142, v142, s31, v135
	v_med3_f32 v136, v136, s31, v135
	v_cvt_pk_fp8_f32 v131, v142, v136 op_sel:[0,0,1]
	v_or_b32_e32 v136, s36, v144
	v_lshlrev_b32_e32 v136, 10, v136
	v_lshl_add_u64 v[142:143], v[136:137], 0, s[2:3]
	v_lshl_add_u64 v[142:143], v[138:139], 0, v[142:143]
	global_store_dwordx4 v[142:143], v[128:131], off
	s_cbranch_vccnz .LBB0_467
	s_cmpk_gt_i32 s34, 0x1fff
	s_cbranch_scc1 .LBB0_480
	s_add_u32 s10, s0, s17
	s_addc_u32 s11, s1, 0
	s_load_dwordx2 s[10:11], s[10:11], 0x0
	s_lshr_b32 s12, s23, 9
	s_mov_b32 s13, s3
	s_add_i32 s12, s12, 2
	s_lshl_b64 s[12:13], s[12:13], 22
	v_add_u32_e32 v0, s2, v132
	s_waitcnt lgkmcnt(0)
	s_add_u32 s10, s10, s12
	v_ashrrev_i32_e32 v1, 31, v0
	s_addc_u32 s11, s11, s13
	s_and_b32 s12, s19, 0x3e0
	v_lshlrev_b64 v[0:1], 12, v[0:1]
	v_lshl_add_u64 v[0:1], s[10:11], 0, v[0:1]
	s_lshl_b32 s2, s12, 2
	v_lshl_add_u64 v[0:1], v[0:1], 0, s[2:3]
	v_lshlrev_b32_e32 v136, 2, v134
	v_lshl_add_u64 v[56:57], v[0:1], 0, v[136:137]
	v_add_co_u32_e32 v8, vcc, s24, v56
	s_nop 1
	v_addc_co_u32_e32 v9, vcc, 0, v57, vcc
	v_add_co_u32_e32 v16, vcc, s25, v56
	global_load_dwordx4 v[0:3], v[8:9], off offset:-4096 nt
	global_load_dwordx4 v[4:7], v[8:9], off nt
	v_addc_co_u32_e32 v17, vcc, 0, v57, vcc
	v_add_co_u32_e32 v24, vcc, s26, v56
	global_load_dwordx4 v[8:11], v[16:17], off offset:-4096 nt
	global_load_dwordx4 v[12:15], v[16:17], off nt
	v_addc_co_u32_e32 v25, vcc, 0, v57, vcc
	v_add_co_u32_e32 v28, vcc, s27, v56
	global_load_dwordx4 v[16:19], v[24:25], off offset:-4096 nt
	global_load_dwordx4 v[20:23], v[24:25], off nt
	v_addc_co_u32_e32 v29, vcc, 0, v57, vcc
	global_load_dwordx4 v[24:27], v[28:29], off offset:-4096 nt
	global_load_dwordx4 v[32:35], v[28:29], off nt
	v_add_co_u32_e32 v28, vcc, s28, v56
	s_nop 1
	v_addc_co_u32_e32 v29, vcc, 0, v57, vcc
	global_load_dwordx4 v[36:39], v[28:29], off offset:-4096 nt
	global_load_dwordx4 v[40:43], v[28:29], off nt
	v_add_co_u32_e32 v28, vcc, s30, v56
	s_nop 1
	v_addc_co_u32_e32 v29, vcc, 0, v57, vcc
	v_add_co_u32_e32 v52, vcc, 0xd000, v56
	global_load_dwordx4 v[44:47], v[28:29], off offset:-4096 nt
	global_load_dwordx4 v[48:51], v[28:29], off nt
	v_addc_co_u32_e32 v53, vcc, 0, v57, vcc
	v_add_co_u32_e32 v58, vcc, 0xe000, v56
	global_load_dwordx4 v[28:31], v[56:57], off nt
	s_nop 0
	global_load_dwordx4 v[52:55], v[52:53], off nt
	v_addc_co_u32_e32 v59, vcc, 0, v57, vcc
	v_add_co_u32_e32 v60, vcc, 0xf000, v56
	s_nop 1
	v_addc_co_u32_e32 v61, vcc, 0, v57, vcc
	global_load_dwordx4 v[56:59], v[58:59], off nt
	s_nop 0
	global_load_dwordx4 v[60:63], v[60:61], off nt

.LBB0_740:
	s_load_dwordx4 s[0:3], s[8:9], 0x138
	s_waitcnt lgkmcnt(0)
	s_mov_b64 s[4:5], s[0:1]
	s_cmp_lt_i32 s4, 7
	s_cselect_b64 s[0:1], -1, 0
	s_cmp_gt_i32 s5, 6
	s_cselect_b64 s[2:3], -1, 0
	s_and_b64 s[0:1], s[0:1], s[2:3]
	s_andn2_b64 vcc, exec, s[0:1]
	s_cbranch_vccnz .LBB0_960
	s_mov_b64 s[0:1], s[8:9]
	v_mbcnt_lo_u32_b32 v135, -1, 0
	v_mbcnt_hi_u32_b32 v135, -1, v135
	s_load_dword s74, s[8:9], 0x148
	s_add_u32 s2, s8, 0x148
	v_readlane_b32 s4, v243, 0
	s_addc_u32 s3, s9, 0
	v_readlane_b32 s5, v243, 1
	s_waitcnt lgkmcnt(0)
	s_sub_i32 s18, s74, 32
	s_cmp_lt_i32 s4, s18
	s_mov_b64 s[4:5], -1
	s_cbranch_scc1 .LBB0_777
	v_readlane_b32 s4, v243, 0
	s_sub_i32 s4, s4, s18
	s_lshl_b32 s4, s4, 3
	s_add_i32 s19, s4, s94
	s_cmpk_gt_u32 s19, 0x3fff
	v_lshlrev_b32_e32 v141, 1, v135
	v_lshlrev_b32_e32 v140, 2, v135
	v_readlane_b32 s5, v243, 1
	s_cbranch_scc1 .LBB0_753
	s_load_dwordx2 s[4:5], s[0:1], 0x118
	s_load_dwordx2 s[8:9], s[0:1], 0x130
	s_lshl_b32 s6, s19, 14
	s_and_b32 s6, s6, 0x7c00000
	v_and_b32_e32 v132, -16, v141
	s_waitcnt lgkmcnt(0)
	s_add_u32 s10, s4, s6
	s_addc_u32 s11, s5, 0
	s_lshl_b32 s20, s19, 2
	s_and_b32 s6, s20, 0x380
	s_waitcnt vmcnt(0)
	v_add_u32_e32 v0, s6, v132
	v_ashrrev_i32_e32 v1, 31, v0
	v_lshlrev_b64 v[0:1], 12, v[0:1]
	s_lshl_b32 s6, s19, 7
	s_mov_b32 s7, 0
	v_lshl_add_u64 v[0:1], s[10:11], 0, v[0:1]
	s_and_b32 s6, s6, 0xf80
	v_and_b32_e32 v134, 28, v140
	v_lshl_add_u64 v[0:1], v[0:1], 0, s[6:7]
	v_mov_b32_e32 v137, 0
	v_lshlrev_b32_e32 v136, 2, v134
	v_lshl_add_u64 v[64:65], v[0:1], 0, v[136:137]
	s_movk_i32 s21, 0x2000
	v_add_co_u32_e32 v8, vcc, s21, v64
	s_movk_i32 s22, 0x4000
	s_nop 0
	v_addc_co_u32_e32 v9, vcc, 0, v65, vcc
	v_add_co_u32_e32 v16, vcc, s22, v64
	s_movk_i32 s23, 0x6000
	s_nop 0
	v_addc_co_u32_e32 v17, vcc, 0, v65, vcc
	v_add_co_u32_e32 v24, vcc, s23, v64
	s_mov_b32 s24, 0x8000
	s_nop 0
	v_addc_co_u32_e32 v25, vcc, 0, v65, vcc
	v_add_co_u32_e32 v32, vcc, s24, v64
	s_mov_b32 s25, 0xa000
	s_nop 0
	v_addc_co_u32_e32 v33, vcc, 0, v65, vcc
	v_add_co_u32_e32 v40, vcc, s25, v64
	s_mov_b32 s26, 0xc000
	s_nop 0
	v_addc_co_u32_e32 v41, vcc, 0, v65, vcc
	v_add_co_u32_e32 v48, vcc, s26, v64
	s_mov_b32 s6, 0xe000
	s_nop 0
	v_addc_co_u32_e32 v49, vcc, 0, v65, vcc
	v_add_co_u32_e32 v52, vcc, s6, v64
	s_mov_b32 s6, 0xf000
	s_nop 0
	v_addc_co_u32_e32 v53, vcc, 0, v65, vcc
	v_add_co_u32_e32 v66, vcc, s6, v64
	global_load_dwordx4 v[0:3], v[8:9], off offset:-4096 nt
	global_load_dwordx4 v[4:7], v[8:9], off nt
	s_nop 0
	global_load_dwordx4 v[8:11], v[16:17], off offset:-4096 nt
	global_load_dwordx4 v[12:15], v[16:17], off nt
	s_nop 0
	global_load_dwordx4 v[16:19], v[24:25], off offset:-4096 nt
	global_load_dwordx4 v[20:23], v[24:25], off nt
	s_nop 0
	global_load_dwordx4 v[24:27], v[32:33], off offset:-4096 nt
	global_load_dwordx4 v[28:31], v[32:33], off nt
	s_nop 0
	global_load_dwordx4 v[32:35], v[40:41], off offset:-4096 nt
	global_load_dwordx4 v[36:39], v[40:41], off nt
	s_nop 0
	global_load_dwordx4 v[40:43], v[48:49], off offset:-4096 nt
	global_load_dwordx4 v[44:47], v[48:49], off nt
	s_nop 0
	global_load_dwordx4 v[48:51], v[52:53], off offset:-4096 nt
	global_load_dwordx4 v[56:59], v[52:53], off nt
	v_addc_co_u32_e32 v67, vcc, 0, v65, vcc
	global_load_dwordx4 v[52:55], v[64:65], off nt
	global_load_dwordx4 v[60:63], v[66:67], off nt
	s_lshl_b32 s27, s19, 5
	s_add_u32 s29, s8, 0x2900000
	v_readlane_b32 s10, v243, 0
	s_addc_u32 s30, s9, 0
	s_lshl_b32 s6, s10, 3
	s_add_i32 s6, s94, s6
	s_lshl_b32 s10, s74, 3
	s_sub_i32 s6, s6, s10
	s_add_i32 s31, s6, 0x300
	s_lshr_b32 s6, s19, 8
	s_mul_hi_u32 s10, s6, 0x300000
	s_mul_i32 s6, s6, 0x300000
	s_add_u32 s8, s8, s6
	v_ashrrev_i32_e32 v133, 31, v132
	v_lshlrev_b32_e32 v64, 6, v135
	s_addc_u32 s9, s9, s10
	v_and_b32_e32 v142, 0x80, v64
	v_readlane_b32 s11, v243, 1
	v_lshl_add_u64 v[64:65], s[8:9], 0, v[132:133]
	s_mov_b64 s[8:9], 0x2b00c00
	s_mov_b32 s28, 0xb000
	v_lshl_add_u64 v[138:139], v[64:65], 0, s[8:9]
	s_mov_b32 s34, 0xc3e00000
	s_mov_b64 s[8:9], 0x200000
	s_mov_b32 s35, 0x200000
	s_mov_b64 s[10:11], 0x600000
	v_mov_b32_e32 v143, 0x304
	v_mov_b32_e32 v144, 0x43e00000
	s_branch .LBB0_746
.LBB0_744:
	v_mul_f32_e32 v128, 0x42000000, v108
	v_mul_f32_e32 v129, 0x42000000, v68
	v_med3_f32 v131, v128, s34, v144
	v_med3_f32 v129, v129, s34, v144
	v_mov_b32_e32 v128, v137
	v_cvt_pk_fp8_f32 v128, v131, v129
	v_mul_f32_e32 v130, 0x42000000, v64
	v_mul_f32_e32 v129, 0x42000000, v76
	v_med3_f32 v130, v130, s34, v144
	v_med3_f32 v129, v129, s34, v144
	v_cvt_pk_fp8_f32 v128, v130, v129 op_sel:[0,0,1]
	v_mul_f32_e32 v129, 0x42000000, v72
	v_mul_f32_e32 v130, 0x42000000, v84
	v_med3_f32 v145, v129, s34, v144
	v_med3_f32 v130, v130, s34, v144
	v_mov_b32_e32 v129, v137
	v_cvt_pk_fp8_f32 v129, v145, v130
	v_mul_f32_e32 v131, 0x42000000, v80
	v_mul_f32_e32 v130, 0x42000000, v92
	v_med3_f32 v131, v131, s34, v144
	v_med3_f32 v130, v130, s34, v144
	v_cvt_pk_fp8_f32 v129, v131, v130 op_sel:[0,0,1]
	v_mul_f32_e32 v130, 0x42000000, v88
	v_mul_f32_e32 v131, 0x42000000, v100
	v_med3_f32 v148, v130, s34, v144
	v_med3_f32 v131, v131, s34, v144
	v_mov_b32_e32 v130, v137
	v_cvt_pk_fp8_f32 v130, v148, v131
	v_mul_f32_e32 v145, 0x42000000, v96
	v_mul_f32_e32 v131, 0x42000000, v104
	s_lshr_b32 s12, s16, 8
	v_med3_f32 v145, v145, s34, v144
	v_med3_f32 v131, v131, s34, v144
	s_mul_hi_u32 s13, s12, 0x300000
	s_mul_i32 s12, s12, 0x300000
	v_cvt_pk_fp8_f32 v130, v145, v131 op_sel:[0,0,1]
	v_mul_f32_e32 v131, 0x42000000, v112
	v_mul_f32_e32 v145, 0x42000000, v116
	s_add_u32 s12, s29, s12
	v_med3_f32 v149, v131, s34, v144
	v_med3_f32 v145, v145, s34, v144
	v_mov_b32_e32 v131, v137
	s_addc_u32 s13, s30, s13
	v_cvt_pk_fp8_f32 v131, v149, v145
	s_add_u32 s12, s12, s6
	s_addc_u32 s13, s13, 0
	v_mul_f32_e32 v148, 0x42000000, v120
	v_mul_f32_e32 v145, 0x42000000, v124
	v_lshl_add_u64 v[146:147], s[12:13], 0, v[132:133]
	v_med3_f32 v148, v148, s34, v144
	v_med3_f32 v145, v145, s34, v144
	v_cvt_pk_fp8_f32 v131, v148, v145 op_sel:[0,0,1]
	v_lshl_add_u64 v[146:147], v[146:147], 0, v[136:137]
	v_mul_f32_e32 v136, 0x42000000, v109
	v_mul_f32_e32 v145, 0x42000000, v69
	v_lshl_add_u64 v[158:159], v[146:147], 0, s[8:9]
	v_add_co_u32_e32 v160, vcc, s35, v146
	v_med3_f32 v136, v136, s34, v144
	v_med3_f32 v145, v145, s34, v144
	v_mov_b32_e32 v146, v137
	v_cvt_pk_fp8_f32 v146, v136, v145
	v_addc_co_u32_e32 v161, vcc, 0, v147, vcc
	v_mul_f32_e32 v147, 0x42000000, v65
	v_mul_f32_e32 v136, 0x42000000, v77
	v_med3_f32 v145, v147, s34, v144
	v_med3_f32 v136, v136, s34, v144
	v_cvt_pk_fp8_f32 v146, v145, v136 op_sel:[0,0,1]
	v_mul_f32_e32 v136, 0x42000000, v73
	v_mul_f32_e32 v145, 0x42000000, v85
	v_med3_f32 v136, v136, s34, v144
	v_med3_f32 v145, v145, s34, v144
	v_mov_b32_e32 v147, v137
	v_cvt_pk_fp8_f32 v147, v136, v145
	v_mul_f32_e32 v148, 0x42000000, v81
	v_mul_f32_e32 v136, 0x42000000, v93
	v_med3_f32 v145, v148, s34, v144
	v_med3_f32 v136, v136, s34, v144
	v_cvt_pk_fp8_f32 v147, v145, v136 op_sel:[0,0,1]
	v_mul_f32_e32 v136, 0x42000000, v89
	v_mul_f32_e32 v145, 0x42000000, v101
	v_med3_f32 v136, v136, s34, v144
	v_med3_f32 v145, v145, s34, v144
	v_mov_b32_e32 v148, v137
	v_cvt_pk_fp8_f32 v148, v136, v145
	v_mul_f32_e32 v149, 0x42000000, v97
	v_mul_f32_e32 v136, 0x42000000, v105
	v_med3_f32 v145, v149, s34, v144
	v_med3_f32 v136, v136, s34, v144
	v_cvt_pk_fp8_f32 v148, v145, v136 op_sel:[0,0,1]
	v_mul_f32_e32 v136, 0x42000000, v113
	v_mul_f32_e32 v145, 0x42000000, v117
	v_med3_f32 v136, v136, s34, v144
	v_med3_f32 v145, v145, s34, v144
	v_mov_b32_e32 v149, v137
	v_cvt_pk_fp8_f32 v149, v136, v145
	v_mul_f32_e32 v150, 0x42000000, v121
	v_mul_f32_e32 v136, 0x42000000, v125
	v_med3_f32 v145, v150, s34, v144
	v_med3_f32 v136, v136, s34, v144
	v_cvt_pk_fp8_f32 v149, v145, v136 op_sel:[0,0,1]
	v_mul_f32_e32 v136, 0x42000000, v110
	v_mul_f32_e32 v145, 0x42000000, v70
	v_med3_f32 v136, v136, s34, v144
	v_med3_f32 v145, v145, s34, v144
	v_mov_b32_e32 v150, v137
	v_cvt_pk_fp8_f32 v150, v136, v145
	v_mul_f32_e32 v151, 0x42000000, v66
	v_mul_f32_e32 v136, 0x42000000, v78
	v_med3_f32 v145, v151, s34, v144
	v_med3_f32 v136, v136, s34, v144
	v_cvt_pk_fp8_f32 v150, v145, v136 op_sel:[0,0,1]
	v_mul_f32_e32 v136, 0x42000000, v74
	v_mul_f32_e32 v145, 0x42000000, v86
	v_med3_f32 v136, v136, s34, v144
	v_med3_f32 v145, v145, s34, v144
	v_mov_b32_e32 v151, v137
	v_cvt_pk_fp8_f32 v151, v136, v145
	v_mul_f32_e32 v152, 0x42000000, v82
	v_mul_f32_e32 v136, 0x42000000, v94
	v_med3_f32 v145, v152, s34, v144
	v_med3_f32 v136, v136, s34, v144
	v_cvt_pk_fp8_f32 v151, v145, v136 op_sel:[0,0,1]
	v_mul_f32_e32 v136, 0x42000000, v90
	v_mul_f32_e32 v145, 0x42000000, v102
	v_med3_f32 v136, v136, s34, v144
	v_med3_f32 v145, v145, s34, v144
	v_mov_b32_e32 v152, v137
	v_cvt_pk_fp8_f32 v152, v136, v145
	v_mul_f32_e32 v153, 0x42000000, v98
	v_mul_f32_e32 v136, 0x42000000, v106
	v_med3_f32 v145, v153, s34, v144
	v_med3_f32 v136, v136, s34, v144
	v_cvt_pk_fp8_f32 v152, v145, v136 op_sel:[0,0,1]
	v_mul_f32_e32 v136, 0x42000000, v114
	v_mul_f32_e32 v145, 0x42000000, v118
	v_med3_f32 v136, v136, s34, v144
	v_med3_f32 v145, v145, s34, v144
	v_mov_b32_e32 v153, v137
	v_cvt_pk_fp8_f32 v153, v136, v145
	v_mul_f32_e32 v154, 0x42000000, v122
	v_mul_f32_e32 v136, 0x42000000, v126
	v_med3_f32 v145, v154, s34, v144
	v_med3_f32 v136, v136, s34, v144
	v_cvt_pk_fp8_f32 v153, v145, v136 op_sel:[0,0,1]
	v_mul_f32_e32 v136, 0x42000000, v111
	v_mul_f32_e32 v145, 0x42000000, v71
	v_med3_f32 v136, v136, s34, v144
	v_med3_f32 v145, v145, s34, v144
	v_mov_b32_e32 v154, v137
	v_cvt_pk_fp8_f32 v154, v136, v145
	v_mul_f32_e32 v155, 0x42000000, v67
	v_mul_f32_e32 v136, 0x42000000, v79
	v_med3_f32 v145, v155, s34, v144
	v_med3_f32 v136, v136, s34, v144
	v_cvt_pk_fp8_f32 v154, v145, v136 op_sel:[0,0,1]
	v_mul_f32_e32 v136, 0x42000000, v75
	v_mul_f32_e32 v145, 0x42000000, v87
	v_med3_f32 v136, v136, s34, v144
	v_med3_f32 v145, v145, s34, v144
	v_mov_b32_e32 v155, v137
	v_cvt_pk_fp8_f32 v155, v136, v145
	v_mul_f32_e32 v156, 0x42000000, v83
	v_mul_f32_e32 v136, 0x42000000, v95
	v_med3_f32 v145, v156, s34, v144
	v_med3_f32 v136, v136, s34, v144
	v_cvt_pk_fp8_f32 v155, v145, v136 op_sel:[0,0,1]
	v_mul_f32_e32 v136, 0x42000000, v91
	v_mul_f32_e32 v145, 0x42000000, v103
	v_med3_f32 v136, v136, s34, v144
	v_med3_f32 v145, v145, s34, v144
	v_mov_b32_e32 v156, v137
	v_cvt_pk_fp8_f32 v156, v136, v145
	v_mul_f32_e32 v157, 0x42000000, v99
	v_mul_f32_e32 v136, 0x42000000, v107
	v_med3_f32 v145, v157, s34, v144
	v_med3_f32 v136, v136, s34, v144
	v_cvt_pk_fp8_f32 v156, v145, v136 op_sel:[0,0,1]
	v_mul_f32_e32 v136, 0x42000000, v115
	v_mul_f32_e32 v145, 0x42000000, v119
	v_med3_f32 v136, v136, s34, v144
	v_med3_f32 v145, v145, s34, v144
	v_mov_b32_e32 v157, v137
	v_cvt_pk_fp8_f32 v157, v136, v145
	v_mul_f32_e32 v162, 0x42000000, v123
	v_mul_f32_e32 v136, 0x42000000, v127
	s_addk_i32 s31, 0x200
	s_addk_i32 s20, 0x800
	s_addk_i32 s27, 0x4000
	v_med3_f32 v145, v162, s34, v144
	v_med3_f32 v136, v136, s34, v144
	s_cmpk_gt_i32 s36, 0x3dff
	v_cvt_pk_fp8_f32 v157, v145, v136 op_sel:[0,0,1]
	v_lshl_add_u64 v[138:139], v[138:139], 0, s[10:11]
	s_cselect_b64 s[14:15], -1, 0
	global_store_dwordx4 v[160:161], v[128:131], off
	global_store_dwordx4 v[158:159], v[146:149], off offset:1024
	global_store_dwordx4 v[158:159], v[150:153], off offset:2048
	global_store_dwordx4 v[158:159], v[154:157], off offset:3072

.LBB0_746:
	s_add_i32 s36, s31, 0xfffffe00
	s_cmpk_lt_i32 s36, 0x3f00
	s_cselect_b64 s[14:15], -1, 0
	s_mov_b64 s[16:17], -1
	s_and_b64 vcc, exec, s[14:15]
	s_cbranch_vccnz .LBB0_748
	s_and_b32 s6, s20, 0x380
	s_and_b32 s12, s27, 0x3e0
	s_mov_b64 s[16:17], 0

.LBB0_750:
	v_or_b32_e32 v128, s12, v134
	v_lshrrev_b32_e32 v128, 1, v128
	v_and_b32_e32 v128, 0x78, v128
	v_bitop3_b32 v129, s12, v143, v134 bitop3:0xc8
	v_or3_b32 v136, v142, v129, v128
	s_waitcnt vmcnt(1)
	v_mul_f32_e32 v128, 0x42000000, v52
	v_mul_f32_e32 v129, 0x42000000, v0
	v_med3_f32 v131, v128, s34, v144
	v_med3_f32 v129, v129, s34, v144
	v_mov_b32_e32 v128, v137
	v_cvt_pk_fp8_f32 v128, v131, v129
	v_mul_f32_e32 v130, 0x42000000, v4
	v_mul_f32_e32 v129, 0x42000000, v8
	v_med3_f32 v130, v130, s34, v144
	v_med3_f32 v129, v129, s34, v144
	v_cvt_pk_fp8_f32 v128, v130, v129 op_sel:[0,0,1]
	v_mul_f32_e32 v129, 0x42000000, v12
	v_mul_f32_e32 v130, 0x42000000, v16
	v_med3_f32 v145, v129, s34, v144
	v_med3_f32 v130, v130, s34, v144
	v_mov_b32_e32 v129, v137
	v_cvt_pk_fp8_f32 v129, v145, v130
	v_mul_f32_e32 v131, 0x42000000, v20
	v_mul_f32_e32 v130, 0x42000000, v24
	v_med3_f32 v131, v131, s34, v144
	v_med3_f32 v130, v130, s34, v144
	v_cvt_pk_fp8_f32 v129, v131, v130 op_sel:[0,0,1]
	v_mul_f32_e32 v130, 0x42000000, v28
	v_mul_f32_e32 v131, 0x42000000, v32
	v_med3_f32 v146, v130, s34, v144
	v_med3_f32 v131, v131, s34, v144
	v_mov_b32_e32 v130, v137
	v_cvt_pk_fp8_f32 v130, v146, v131
	v_mul_f32_e32 v145, 0x42000000, v36
	v_mul_f32_e32 v131, 0x42000000, v40
	v_med3_f32 v145, v145, s34, v144
	v_med3_f32 v131, v131, s34, v144
	v_cvt_pk_fp8_f32 v130, v145, v131 op_sel:[0,0,1]
	v_mul_f32_e32 v131, 0x42000000, v44
	v_mul_f32_e32 v145, 0x42000000, v48
	v_med3_f32 v147, v131, s34, v144
	v_med3_f32 v145, v145, s34, v144
	v_mov_b32_e32 v131, v137
	v_cvt_pk_fp8_f32 v131, v147, v145
	v_mul_f32_e32 v146, 0x42000000, v56
	s_waitcnt vmcnt(0)
	v_mul_f32_e32 v145, 0x42000000, v60
	v_med3_f32 v146, v146, s34, v144
	v_med3_f32 v145, v145, s34, v144
	v_lshlrev_b32_e32 v136, 10, v136
	v_cvt_pk_fp8_f32 v131, v146, v145 op_sel:[0,0,1]
	v_lshl_add_u64 v[146:147], v[136:137], 0, s[6:7]
	v_lshl_add_u64 v[158:159], v[138:139], 0, v[146:147]
	v_mul_f32_e32 v145, 0x42000000, v53
	v_mul_f32_e32 v146, 0x42000000, v1
	v_med3_f32 v145, v145, s34, v144
	v_med3_f32 v148, v146, s34, v144
	v_mov_b32_e32 v146, v137
	v_cvt_pk_fp8_f32 v146, v145, v148
	v_mul_f32_e32 v147, 0x42000000, v5
	v_mul_f32_e32 v145, 0x42000000, v9
	v_med3_f32 v147, v147, s34, v144
	v_med3_f32 v145, v145, s34, v144
	v_cvt_pk_fp8_f32 v146, v147, v145 op_sel:[0,0,1]
	v_mul_f32_e32 v145, 0x42000000, v13
	v_mul_f32_e32 v147, 0x42000000, v17
	v_med3_f32 v145, v145, s34, v144
	v_med3_f32 v149, v147, s34, v144
	v_mov_b32_e32 v147, v137
	v_cvt_pk_fp8_f32 v147, v145, v149
	v_mul_f32_e32 v148, 0x42000000, v21
	v_mul_f32_e32 v145, 0x42000000, v25
	v_med3_f32 v148, v148, s34, v144
	v_med3_f32 v145, v145, s34, v144
	v_cvt_pk_fp8_f32 v147, v148, v145 op_sel:[0,0,1]
	v_mul_f32_e32 v145, 0x42000000, v29
	v_mul_f32_e32 v148, 0x42000000, v33
	v_med3_f32 v145, v145, s34, v144
	v_med3_f32 v150, v148, s34, v144
	v_mov_b32_e32 v148, v137
	v_cvt_pk_fp8_f32 v148, v145, v150
	v_mul_f32_e32 v149, 0x42000000, v37
	v_mul_f32_e32 v145, 0x42000000, v41
	v_med3_f32 v149, v149, s34, v144
	v_med3_f32 v145, v145, s34, v144
	v_cvt_pk_fp8_f32 v148, v149, v145 op_sel:[0,0,1]
	v_mul_f32_e32 v145, 0x42000000, v45
	v_mul_f32_e32 v149, 0x42000000, v49
	v_med3_f32 v145, v145, s34, v144
	v_med3_f32 v151, v149, s34, v144
	v_mov_b32_e32 v149, v137
	v_cvt_pk_fp8_f32 v149, v145, v151
	v_mul_f32_e32 v150, 0x42000000, v57
	v_mul_f32_e32 v145, 0x42000000, v61
	v_med3_f32 v150, v150, s34, v144
	v_med3_f32 v145, v145, s34, v144
	v_cvt_pk_fp8_f32 v149, v150, v145 op_sel:[0,0,1]
	v_mul_f32_e32 v145, 0x42000000, v54
	v_mul_f32_e32 v150, 0x42000000, v2
	v_med3_f32 v145, v145, s34, v144
	v_med3_f32 v152, v150, s34, v144
	v_mov_b32_e32 v150, v137
	v_cvt_pk_fp8_f32 v150, v145, v152
	v_mul_f32_e32 v151, 0x42000000, v6
	v_mul_f32_e32 v145, 0x42000000, v10
	v_med3_f32 v151, v151, s34, v144
	v_med3_f32 v145, v145, s34, v144
	v_cvt_pk_fp8_f32 v150, v151, v145 op_sel:[0,0,1]
	v_mul_f32_e32 v145, 0x42000000, v14
	v_mul_f32_e32 v151, 0x42000000, v18
	v_med3_f32 v145, v145, s34, v144
	v_med3_f32 v153, v151, s34, v144
	v_mov_b32_e32 v151, v137
	v_cvt_pk_fp8_f32 v151, v145, v153
	v_mul_f32_e32 v152, 0x42000000, v22
	v_mul_f32_e32 v145, 0x42000000, v26
	v_med3_f32 v152, v152, s34, v144
	v_med3_f32 v145, v145, s34, v144
	v_cvt_pk_fp8_f32 v151, v152, v145 op_sel:[0,0,1]
	v_mul_f32_e32 v145, 0x42000000, v30
	v_mul_f32_e32 v152, 0x42000000, v34
	v_med3_f32 v145, v145, s34, v144
	v_med3_f32 v154, v152, s34, v144
	v_mov_b32_e32 v152, v137
	v_cvt_pk_fp8_f32 v152, v145, v154
	v_mul_f32_e32 v153, 0x42000000, v38
	v_mul_f32_e32 v145, 0x42000000, v42
	v_med3_f32 v153, v153, s34, v144
	v_med3_f32 v145, v145, s34, v144
	v_cvt_pk_fp8_f32 v152, v153, v145 op_sel:[0,0,1]
	v_mul_f32_e32 v145, 0x42000000, v46
	v_mul_f32_e32 v153, 0x42000000, v50
	v_med3_f32 v145, v145, s34, v144
	v_med3_f32 v155, v153, s34, v144
	v_mov_b32_e32 v153, v137
	v_cvt_pk_fp8_f32 v153, v145, v155
	v_mul_f32_e32 v154, 0x42000000, v58
	v_mul_f32_e32 v145, 0x42000000, v62
	v_med3_f32 v154, v154, s34, v144
	v_med3_f32 v145, v145, s34, v144
	v_cvt_pk_fp8_f32 v153, v154, v145 op_sel:[0,0,1]
	v_mul_f32_e32 v145, 0x42000000, v55
	v_mul_f32_e32 v154, 0x42000000, v3
	v_med3_f32 v145, v145, s34, v144
	v_med3_f32 v156, v154, s34, v144
	v_mov_b32_e32 v154, v137
	v_cvt_pk_fp8_f32 v154, v145, v156
	v_mul_f32_e32 v155, 0x42000000, v7
	v_mul_f32_e32 v145, 0x42000000, v11
	v_med3_f32 v155, v155, s34, v144
	v_med3_f32 v145, v145, s34, v144
	v_cvt_pk_fp8_f32 v154, v155, v145 op_sel:[0,0,1]
	v_mul_f32_e32 v145, 0x42000000, v15
	v_mul_f32_e32 v155, 0x42000000, v19
	v_med3_f32 v145, v145, s34, v144
	v_med3_f32 v157, v155, s34, v144
	v_mov_b32_e32 v155, v137
	v_cvt_pk_fp8_f32 v155, v145, v157
	v_mul_f32_e32 v156, 0x42000000, v23
	v_mul_f32_e32 v145, 0x42000000, v27
	v_med3_f32 v156, v156, s34, v144
	v_med3_f32 v145, v145, s34, v144
	v_cvt_pk_fp8_f32 v155, v156, v145 op_sel:[0,0,1]
	v_mul_f32_e32 v145, 0x42000000, v31
	v_mul_f32_e32 v156, 0x42000000, v35
	v_med3_f32 v145, v145, s34, v144
	v_med3_f32 v160, v156, s34, v144
	v_mov_b32_e32 v156, v137
	v_cvt_pk_fp8_f32 v156, v145, v160
	v_mul_f32_e32 v157, 0x42000000, v39
	v_mul_f32_e32 v145, 0x42000000, v43
	v_med3_f32 v157, v157, s34, v144
	v_med3_f32 v145, v145, s34, v144
	v_cvt_pk_fp8_f32 v156, v157, v145 op_sel:[0,0,1]
	v_mul_f32_e32 v145, 0x42000000, v47
	v_mul_f32_e32 v157, 0x42000000, v51
	v_med3_f32 v145, v145, s34, v144
	v_med3_f32 v161, v157, s34, v144
	v_mov_b32_e32 v157, v137
	v_cvt_pk_fp8_f32 v157, v145, v161
	v_mul_f32_e32 v160, 0x42000000, v59
	v_mul_f32_e32 v145, 0x42000000, v63
	v_med3_f32 v160, v160, s34, v144
	v_med3_f32 v145, v145, s34, v144
	v_cvt_pk_fp8_f32 v157, v160, v145 op_sel:[0,0,1]
	s_andn2_b64 vcc, exec, s[14:15]
	s_mov_b64 s[14:15], -1
	global_store_dwordx4 v[158:159], v[128:131], off offset:-3072
	global_store_dwordx4 v[158:159], v[146:149], off offset:-2048
	global_store_dwordx4 v[158:159], v[150:153], off offset:-1024
	global_store_dwordx4 v[158:159], v[154:157], off
	s_cbranch_vccnz .LBB0_745
	s_cmpk_gt_i32 s36, 0x3dff
	s_cbranch_scc1 .LBB0_744
	s_lshr_b32 s14, s31, 8
	s_mov_b32 s15, s7
	s_lshl_b64 s[14:15], s[14:15], 22
	v_add_u32_e32 v0, s6, v132
	s_add_u32 s14, s4, s14
	v_ashrrev_i32_e32 v1, 31, v0
	s_addc_u32 s15, s5, s15
	v_lshlrev_b64 v[0:1], 12, v[0:1]
	v_lshl_add_u64 v[0:1], s[14:15], 0, v[0:1]
	s_mov_b32 s13, s7
	v_lshl_add_u64 v[0:1], s[12:13], 2, v[0:1]
	v_lshlrev_b32_e32 v2, 2, v134
	v_mov_b32_e32 v3, v137
	v_lshl_add_u64 v[56:57], v[0:1], 0, v[2:3]
	v_add_co_u32_e32 v8, vcc, s21, v56
	s_nop 1
	v_addc_co_u32_e32 v9, vcc, 0, v57, vcc
	v_add_co_u32_e32 v16, vcc, s22, v56
	global_load_dwordx4 v[0:3], v[8:9], off offset:-4096 nt
	global_load_dwordx4 v[4:7], v[8:9], off nt
	v_addc_co_u32_e32 v17, vcc, 0, v57, vcc
	v_add_co_u32_e32 v24, vcc, s23, v56
	global_load_dwordx4 v[8:11], v[16:17], off offset:-4096 nt
	global_load_dwordx4 v[12:15], v[16:17], off nt
	v_addc_co_u32_e32 v25, vcc, 0, v57, vcc
	v_add_co_u32_e32 v32, vcc, s24, v56
	global_load_dwordx4 v[16:19], v[24:25], off offset:-4096 nt
	global_load_dwordx4 v[20:23], v[24:25], off nt
	v_addc_co_u32_e32 v33, vcc, 0, v57, vcc
	v_add_co_u32_e32 v40, vcc, s25, v56
	global_load_dwordx4 v[24:27], v[32:33], off offset:-4096 nt
	global_load_dwordx4 v[28:31], v[32:33], off nt
	v_addc_co_u32_e32 v41, vcc, 0, v57, vcc
	v_add_co_u32_e32 v44, vcc, s26, v56
	global_load_dwordx4 v[32:35], v[40:41], off offset:-4096 nt
	global_load_dwordx4 v[36:39], v[40:41], off nt
	v_addc_co_u32_e32 v45, vcc, 0, v57, vcc
	v_add_co_u32_e32 v48, vcc, 0xd000, v56
	global_load_dwordx4 v[40:43], v[44:45], off offset:-4096 nt
	s_nop 0
	global_load_dwordx4 v[44:47], v[44:45], off nt
	v_addc_co_u32_e32 v49, vcc, 0, v57, vcc
	v_add_co_u32_e32 v58, vcc, 0xe000, v56
	global_load_dwordx4 v[52:55], v[56:57], off nt
	s_nop 0
	global_load_dwordx4 v[48:51], v[48:49], off nt
	v_addc_co_u32_e32 v59, vcc, 0, v57, vcc
	v_add_co_u32_e32 v60, vcc, 0xf000, v56
	s_nop 1
	v_addc_co_u32_e32 v61, vcc, 0, v57, vcc
	global_load_dwordx4 v[56:59], v[58:59], off nt
	s_nop 0
	global_load_dwordx4 v[60:63], v[60:61], off nt
	s_branch .LBB0_744
.LBB0_753:
	s_cmp_eq_u32 s19, s19
	s_cbranch_scc1 .LBB0_776
	s_ashr_i32 s6, s19, 31
	s_lshr_b32 s4, s6, 24
	s_add_i32 s11, s19, s4
	s_ashr_i32 s4, s11, 8
	s_lshr_b32 s5, s11, 31
	s_add_i32 s5, s4, s5
	s_and_b32 s5, s5, -2
	s_sub_i32 s4, s4, s5
	s_cmp_eq_u32 s4, 1
	s_movk_i32 s10, 0x108
	s_cselect_b32 s5, s10, 0x118
	s_cmp_lg_u32 s4, 0
	s_cselect_b32 s4, s5, 0xf8
	s_add_u32 s4, s0, s4
	s_addc_u32 s5, s1, 0
	s_load_dwordx2 s[4:5], s[4:5], 0x0
	s_lshr_b32 s6, s6, 23
	s_add_i32 s6, s19, s6
	s_ashr_i32 s6, s6, 9
	s_ashr_i32 s7, s6, 31
	s_lshl_b64 s[6:7], s[6:7], 22
	s_load_dwordx2 s[8:9], s[0:1], 0x130
	s_waitcnt lgkmcnt(0)
	s_add_u32 s4, s4, s6
	s_addc_u32 s5, s5, s7
	s_and_b32 s6, s11, 0xff00
	s_sub_i32 s6, s19, s6
	s_sext_i32_i16 s7, s6
	s_bfe_u32 s7, s7, 0x5001a
	s_add_i32 s7, s6, s7
	s_sext_i32_i16 s11, s7
	s_and_b32 s7, s7, 0xffe0
	s_sub_i32 s6, s6, s7
	s_lshl_b32 s7, s11, 2
	s_and_b32 s7, s7, 0xffffff80
	v_and_b32_e32 v132, -16, v141
	s_waitcnt vmcnt(0)
	v_add_u32_e32 v0, s7, v132
	s_sext_i32_i16 s6, s6
	v_ashrrev_i32_e32 v1, 31, v0
	s_lshl_b32 s6, s6, 5
	v_lshlrev_b64 v[0:1], 12, v[0:1]
	v_lshl_add_u64 v[0:1], s[4:5], 0, v[0:1]
	s_ashr_i32 s7, s6, 31
	v_and_b32_e32 v134, 28, v140
	v_lshl_add_u64 v[0:1], s[6:7], 2, v[0:1]
	v_mov_b32_e32 v137, 0
	v_lshlrev_b32_e32 v136, 2, v134
	v_lshl_add_u64 v[52:53], v[0:1], 0, v[136:137]
	s_mov_b32 s11, 0x8001000
	v_add_co_u32_e32 v8, vcc, s11, v52
	s_mov_b32 s12, 0x8003000
	s_nop 0
	v_addc_co_u32_e32 v9, vcc, 0, v53, vcc
	v_add_co_u32_e32 v16, vcc, s12, v52
	s_mov_b32 s13, 0x8005000
	s_nop 0
	v_addc_co_u32_e32 v17, vcc, 0, v53, vcc
	v_add_co_u32_e32 v24, vcc, s13, v52
	s_mov_b32 s14, 0x8007000
	s_nop 0
	v_addc_co_u32_e32 v25, vcc, 0, v53, vcc
	v_add_co_u32_e32 v32, vcc, s14, v52
	s_mov_b32 s15, 0x8009000
	s_nop 0
	v_addc_co_u32_e32 v33, vcc, 0, v53, vcc
	v_add_co_u32_e32 v40, vcc, s15, v52
	s_mov_b32 s16, 0x800b000
	s_nop 0
	v_addc_co_u32_e32 v41, vcc, 0, v53, vcc
	v_add_co_u32_e32 v48, vcc, s16, v52
	s_mov_b32 s4, 0x800d000
	s_nop 0
	v_addc_co_u32_e32 v49, vcc, 0, v53, vcc
	v_add_co_u32_e32 v54, vcc, s4, v52
	s_mov_b32 s4, 0x800f000
	s_nop 0
	v_addc_co_u32_e32 v55, vcc, 0, v53, vcc
	v_add_co_u32_e32 v52, vcc, s4, v52
	global_load_dwordx4 v[0:3], v[8:9], off offset:-4096 nt
	global_load_dwordx4 v[4:7], v[8:9], off nt
	v_addc_co_u32_e32 v53, vcc, 0, v53, vcc
	global_load_dwordx4 v[8:11], v[16:17], off offset:-4096 nt
	global_load_dwordx4 v[12:15], v[16:17], off nt
	s_nop 0
	global_load_dwordx4 v[16:19], v[24:25], off offset:-4096 nt
	global_load_dwordx4 v[20:23], v[24:25], off nt
	s_nop 0
	global_load_dwordx4 v[24:27], v[32:33], off offset:-4096 nt
	global_load_dwordx4 v[28:31], v[32:33], off nt
	s_nop 0
	global_load_dwordx4 v[32:35], v[40:41], off offset:-4096 nt
	global_load_dwordx4 v[36:39], v[40:41], off nt
	s_nop 0
	global_load_dwordx4 v[40:43], v[48:49], off offset:-4096 nt
	global_load_dwordx4 v[44:47], v[48:49], off nt
	s_nop 0
	global_load_dwordx4 v[48:51], v[54:55], off offset:-4096 nt
	global_load_dwordx4 v[60:63], v[54:55], off nt
	global_load_dwordx4 v[88:91], v[52:53], off offset:-4096 nt
	global_load_dwordx4 v[100:103], v[52:53], off nt
	s_add_u32 s20, s8, 0x2900000
	s_mov_b32 s17, 0x800c000
	s_addc_u32 s21, s9, 0
	v_ashrrev_i32_e32 v133, 31, v132
	s_mov_b32 s22, 0xc3e00000
	s_mov_b64 s[4:5], 0x200000
	v_mov_b32_e32 v142, 0x43e00000
	v_mov_b32_e32 v143, 0xffffff04
	s_branch .LBB0_757

.LBB0_960:
	s_load_dwordx4 s[0:3], s[8:9], 0x138
	s_waitcnt lgkmcnt(0)
	s_mov_b64 s[4:5], s[0:1]
	s_cmp_lt_i32 s4, 8
	s_cselect_b64 s[0:1], -1, 0
	s_cmp_gt_i32 s5, 7
	s_cselect_b64 s[2:3], -1, 0
	s_and_b64 s[0:1], s[0:1], s[2:3]
	s_andn2_b64 vcc, exec, s[0:1]
	s_cbranch_vccnz .LBB0_1169
	s_mov_b64 s[2:3], s[8:9]
	v_mbcnt_lo_u32_b32 v135, -1, 0
	v_mbcnt_hi_u32_b32 v135, -1, v135
	s_load_dword s74, s[8:9], 0x148
	s_add_u32 s0, s8, 0x148
	v_readlane_b32 s4, v243, 0
	s_addc_u32 s1, s9, 0
	v_readlane_b32 s5, v243, 1
	s_waitcnt lgkmcnt(0)
	s_sub_i32 s18, s74, 0
	s_cmp_lt_i32 s4, s18
	s_mov_b64 s[4:5], -1
	s_cbranch_scc1 .LBB0_997
	v_readlane_b32 s4, v243, 0
	s_sub_i32 s4, s4, s18
	s_lshl_b32 s4, s4, 3
	s_add_i32 s19, s4, s94
	s_cmpk_gt_u32 s19, 0x1fff
	v_lshlrev_b32_e32 v141, 1, v135
	v_lshlrev_b32_e32 v140, 2, v135
	v_readlane_b32 s5, v243, 1
	s_cbranch_scc1 .LBB0_973
	s_load_dwordx2 s[4:5], s[2:3], 0x118
	s_load_dwordx2 s[8:9], s[2:3], 0x130
	s_lshl_b32 s6, s19, 14
	s_and_b32 s6, s6, 0x7c00000
	v_and_b32_e32 v132, -16, v141
	s_waitcnt lgkmcnt(0)
	s_add_u32 s10, s4, s6
	s_addc_u32 s11, s5, 0
	s_lshl_b32 s20, s19, 2
	s_and_b32 s6, s20, 0x380
	s_waitcnt vmcnt(0)
	v_add_u32_e32 v0, s6, v132
	v_ashrrev_i32_e32 v1, 31, v0
	v_lshlrev_b64 v[0:1], 12, v[0:1]
	s_lshl_b32 s6, s19, 7
	s_mov_b32 s7, 0
	v_lshl_add_u64 v[0:1], s[10:11], 0, v[0:1]
	s_and_b32 s6, s6, 0xf80
	v_and_b32_e32 v134, 28, v140
	v_lshl_add_u64 v[0:1], v[0:1], 0, s[6:7]
	v_mov_b32_e32 v137, 0
	v_lshlrev_b32_e32 v136, 2, v134
	v_lshl_add_u64 v[56:57], v[0:1], 0, v[136:137]
	s_mov_b32 s6, 0x8001000
	v_add_co_u32_e32 v4, vcc, s6, v56
	s_mov_b32 s6, 0x8003000
	s_nop 0
	v_addc_co_u32_e32 v5, vcc, 0, v57, vcc
	v_add_co_u32_e32 v12, vcc, s6, v56
	s_mov_b32 s6, 0x8005000
	s_nop 0
	v_addc_co_u32_e32 v13, vcc, 0, v57, vcc
	v_add_co_u32_e32 v20, vcc, s6, v56
	s_mov_b32 s6, 0x8007000
	s_nop 0
	v_addc_co_u32_e32 v21, vcc, 0, v57, vcc
	v_add_co_u32_e32 v32, vcc, s6, v56
	s_mov_b32 s6, 0x8009000
	s_nop 0
	v_addc_co_u32_e32 v33, vcc, 0, v57, vcc
	v_add_co_u32_e32 v40, vcc, s6, v56
	s_mov_b32 s6, 0x800b000
	s_nop 0
	v_addc_co_u32_e32 v41, vcc, 0, v57, vcc
	v_add_co_u32_e32 v48, vcc, s6, v56
	s_mov_b32 s6, 0x800d000
	s_nop 0
	v_addc_co_u32_e32 v49, vcc, 0, v57, vcc
	v_add_co_u32_e32 v58, vcc, s6, v56
	s_mov_b32 s6, 0x800f000
	s_nop 0
	v_addc_co_u32_e32 v59, vcc, 0, v57, vcc
	v_add_co_u32_e32 v64, vcc, s6, v56
	global_load_dwordx4 v[24:27], v[4:5], off offset:-4096 nt
	global_load_dwordx4 v[0:3], v[4:5], off nt
	v_addc_co_u32_e32 v65, vcc, 0, v57, vcc
	global_load_dwordx4 v[4:7], v[12:13], off offset:-4096 nt
	global_load_dwordx4 v[8:11], v[12:13], off nt
	s_nop 0
	global_load_dwordx4 v[12:15], v[20:21], off offset:-4096 nt
	global_load_dwordx4 v[16:19], v[20:21], off nt
	s_nop 0
	global_load_dwordx4 v[20:23], v[32:33], off offset:-4096 nt
	global_load_dwordx4 v[28:31], v[32:33], off nt
	s_nop 0
	global_load_dwordx4 v[32:35], v[40:41], off offset:-4096 nt
	global_load_dwordx4 v[36:39], v[40:41], off nt
	s_nop 0
	global_load_dwordx4 v[40:43], v[48:49], off offset:-4096 nt
	global_load_dwordx4 v[44:47], v[48:49], off nt
	s_nop 0
	global_load_dwordx4 v[48:51], v[58:59], off offset:-4096 nt
	global_load_dwordx4 v[52:55], v[58:59], off nt
	s_nop 0
	global_load_dwordx4 v[56:59], v[64:65], off offset:-4096 nt
	global_load_dwordx4 v[60:63], v[64:65], off nt
	s_lshl_b32 s21, s19, 5
	s_add_u32 s22, s8, 0x2900000
	v_readlane_b32 s10, v243, 0
	s_addc_u32 s23, s9, 0
	s_lshl_b32 s6, s10, 3
	s_add_i32 s6, s94, s6
	s_lshl_b32 s10, s74, 3
	s_sub_i32 s6, s6, s10
	s_add_i32 s24, s6, 0x300
	s_lshr_b32 s6, s19, 8
	s_mul_hi_u32 s10, s6, 0x300000
	s_mul_i32 s6, s6, 0x300000
	s_add_u32 s8, s8, s6
	v_ashrrev_i32_e32 v133, 31, v132
	v_lshlrev_b32_e32 v64, 6, v135
	s_addc_u32 s9, s9, s10
	v_and_b32_e32 v142, 0x80, v64
	v_readlane_b32 s11, v243, 1
	v_lshl_add_u64 v[64:65], s[8:9], 0, v[132:133]
	s_mov_b64 s[8:9], 0x8b00c00
	v_lshl_add_u64 v[138:139], v[64:65], 0, s[8:9]
	s_movk_i32 s25, 0x2000
	s_movk_i32 s26, 0x4000
	s_movk_i32 s27, 0x6000
	s_mov_b32 s28, 0x8000
	s_mov_b32 s29, 0xa000
	s_mov_b32 s30, 0xb000
	s_mov_b32 s31, 0xc000
	s_mov_b32 s34, 0xc3e00000
	s_mov_b64 s[8:9], 0x200000
	s_mov_b32 s35, 0x200000
	s_mov_b64 s[10:11], 0x600000
	v_mov_b32_e32 v143, 0x304
	v_mov_b32_e32 v144, 0x43e00000
	s_branch .LBB0_966

.LBB0_1465:
	v_mov_b32_e32 v162, v202
	s_waitcnt vmcnt(0)
	s_or_b64 s[52:53], s[42:43], s[52:53]
	s_ashr_i32 s59, s62, 31
	v_mov_b32_e32 v64, 0
	s_and_b64 vcc, exec, s[52:53]
	v_mov_b32_e32 v65, 0
	v_mov_b32_e32 v66, 0
	v_mov_b32_e32 v67, 0
	v_mov_b32_e32 v68, 0
	v_mov_b32_e32 v69, 0
	v_mov_b32_e32 v70, 0
	v_mov_b32_e32 v71, 0
	v_mov_b32_e32 v163, 0
	v_mov_b32_e32 v209, 0
	v_mov_b32_e32 v210, 0
	v_mov_b32_e32 v211, 0
	v_mov_b32_e32 v212, 0
	v_mov_b32_e32 v213, 0
	v_mov_b32_e32 v214, 0
	v_mov_b32_e32 v215, 0
	s_waitcnt vmcnt(0) lgkmcnt(0)
	s_barrier
	s_cbranch_vccnz .LBB0_1467
	v_add_u32_e32 v68, 64, v162
	s_add_u32 s52, s62, s83
	v_ashrrev_i32_e32 v66, 3, v162
	v_ashrrev_i32_e32 v68, 3, v68
	s_addc_u32 s53, s59, s80
	v_lshlrev_b32_e32 v64, 4, v162
	v_ashrrev_i32_e32 v67, 31, v66
	v_ashrrev_i32_e32 v69, 31, v68
	v_and_b32_e32 v110, 0x70, v64
	v_lshl_add_u64 v[66:67], s[52:53], 0, v[66:67]
	v_lshl_add_u64 v[68:69], s[52:53], 0, v[68:69]
	v_lshl_add_u64 v[64:65], s[38:39], 0, v[110:111]
	v_lshlrev_b64 v[66:67], 11, v[66:67]
	v_lshlrev_b64 v[68:69], 11, v[68:69]
	v_ashrrev_i32_e32 v163, 31, v162
	v_lshl_add_u64 v[66:67], v[64:65], 0, v[66:67]
	v_lshl_add_u64 v[64:65], v[64:65], 0, v[68:69]
	v_lshl_add_u64 v[72:73], v[162:163], 2, s[44:45]
	global_load_dwordx4 v[68:71], v[66:67], off
	s_nop 0
	global_load_dwordx4 v[64:67], v[64:65], off
	s_nop 0
	global_load_dword v163, v[72:73], off offset:-1024
	global_load_dword v209, v[72:73], off offset:-768
	global_load_dword v210, v[72:73], off offset:-512
	global_load_dword v211, v[72:73], off offset:-256
	global_load_dword v212, v[72:73], off
	global_load_dword v213, v[72:73], off offset:256
	global_load_dword v214, v[72:73], off offset:512
	global_load_dword v215, v[72:73], off offset:768
